# plan G: in-proj-0 with 56 conversion WGs (hand-written conversion routine, gate/up le [20,47) + L1 down [48,64)); MoE-up-0 conversion WGs keep down [0,48)
# baseline (speedup 1.0000x reference)
.LBB0_254:
	s_load_dwordx4 s[0:3], s[8:9], 0x138
	s_waitcnt lgkmcnt(0)
	s_mov_b64 s[4:5], s[0:1]
	s_cmp_lt_i32 s4, 3
	s_cselect_b64 s[0:1], -1, 0
	s_cmp_gt_i32 s5, 2
	s_cselect_b64 s[2:3], -1, 0
	s_and_b64 s[0:1], s[0:1], s[2:3]
	s_andn2_b64 vcc, exec, s[0:1]
	s_cbranch_vccnz .LBB0_356
	s_mov_b64 s[0:1], s[8:9]
	v_mbcnt_lo_u32_b32 v152, -1, 0
	v_mbcnt_hi_u32_b32 v152, -1, v152
	s_load_dword s38, s[8:9], 0x148
	s_add_u32 s2, s8, 0x148
	v_readlane_b32 s4, v243, 0
	s_addc_u32 s3, s9, 0
	v_readlane_b32 s5, v243, 1
	s_waitcnt lgkmcnt(0)
	s_sub_i32 s39, s38, 56
	s_cmp_lt_i32 s4, s39
	s_mov_b64 s[4:5], -1
	s_cbranch_scc1 .LBB0_276
	v_readlane_b32 s4, v243, 0
	s_sub_i32 s4, s4, s39
	s_lshl_b32 s4, s4, 3
	s_add_i32 s19, s4, s94
	s_mov_b32 s4, s19
	s_mov_b32 s5, 0x1c0
	s_mov_b32 s6, 0x3600
	s_waitcnt vmcnt(0)
	s_cmp_ge_u32 s4, s6
	s_cbranch_scc1 .Lp2c0_done
	v_readlane_b32 s8, v243, 7
	v_readlane_b32 s9, v243, 8
	s_load_dwordx2 s[10:11], s[8:9], 0x130
	s_load_dwordx2 s[12:13], s[8:9], 0xf8
	s_load_dwordx2 s[14:15], s[8:9], 0x108
	v_mbcnt_lo_u32_b32 v142, -1, 0
	v_mbcnt_hi_u32_b32 v142, -1, v142
	v_lshrrev_b32_e32 v143, 3, v142
	v_and_b32_e32 v142, 7, v142
	v_lshlrev_b32_e32 v136, 16, v143
	v_lshl_add_u32 v136, v142, 4, v136
	v_add_u32_e32 v137, 0x1000, v136
	v_add_u32_e32 v138, 0x2000, v136
	v_add_u32_e32 v139, 0x3000, v136
	v_lshlrev_b32_e32 v140, 12, v142
	v_lshl_add_u32 v140, v143, 4, v140
	v_mov_b32_e32 v141, 0x43e00000
	s_mov_b32 s28, 0xc3e00000
	s_waitcnt lgkmcnt(0)
	s_add_u32 s10, s10, 0x2900000
	s_addc_u32 s11, s11, 0
	s_lshr_b32 s22, s4, 8
	s_and_b32 s23, s4, 0xff
	s_and_b32 s27, s22, 1
	s_lshr_b32 s22, s22, 1
	s_cmp_eq_u32 s27, 0
	s_cselect_b64 s[16:17], s[12:13], s[14:15]
	s_add_i32 s22, s22, 20
	s_lshl_b32 s24, s22, 22
	s_lshr_b32 s25, s23, 5
	s_lshl_b32 s25, s25, 19
	s_and_b32 s26, s23, 31
	s_lshl_b32 s26, s26, 7
	s_add_i32 s24, s24, s25
	s_add_i32 s24, s24, s26
	s_add_u32 s16, s16, s24
	s_addc_u32 s17, s17, 0
	s_nop 0
	global_load_dwordx4 v[0:3], v136, s[16:17] nt
	global_load_dwordx4 v[4:7], v137, s[16:17] nt
	global_load_dwordx4 v[8:11], v138, s[16:17] nt
	global_load_dwordx4 v[12:15], v139, s[16:17] nt
	s_add_u32 s16, s16, 0x4000
	s_addc_u32 s17, s17, 0
	s_nop 0
	global_load_dwordx4 v[16:19], v136, s[16:17] nt
	global_load_dwordx4 v[20:23], v137, s[16:17] nt
	global_load_dwordx4 v[24:27], v138, s[16:17] nt
	global_load_dwordx4 v[28:31], v139, s[16:17] nt
	s_add_u32 s16, s16, 0x4000
	s_addc_u32 s17, s17, 0
	s_nop 0
	global_load_dwordx4 v[32:35], v136, s[16:17] nt
	global_load_dwordx4 v[36:39], v137, s[16:17] nt
	global_load_dwordx4 v[40:43], v138, s[16:17] nt
	global_load_dwordx4 v[44:47], v139, s[16:17] nt
	s_add_u32 s16, s16, 0x4000
	s_addc_u32 s17, s17, 0
	s_nop 0
	global_load_dwordx4 v[48:51], v136, s[16:17] nt
	global_load_dwordx4 v[52:55], v137, s[16:17] nt
	global_load_dwordx4 v[56:59], v138, s[16:17] nt
	global_load_dwordx4 v[60:63], v139, s[16:17] nt
	s_add_i32 s7, s4, s5
	s_cmp_lt_u32 s7, s6
	s_cbranch_scc0 .Lp2c0_p_last
	s_lshr_b32 s22, s7, 8
	s_and_b32 s23, s7, 0xff
	s_and_b32 s27, s22, 1
	s_lshr_b32 s22, s22, 1
	s_cmp_eq_u32 s27, 0
	s_cselect_b64 s[16:17], s[12:13], s[14:15]
	s_add_i32 s22, s22, 20
	s_lshl_b32 s24, s22, 22
	s_lshr_b32 s25, s23, 5
	s_lshl_b32 s25, s25, 19
	s_and_b32 s26, s23, 31
	s_lshl_b32 s26, s26, 7
	s_add_i32 s24, s24, s25
	s_add_i32 s24, s24, s26
	s_add_u32 s16, s16, s24
	s_addc_u32 s17, s17, 0
	s_nop 0
	global_load_dwordx4 v[64:67], v136, s[16:17] nt
	global_load_dwordx4 v[68:71], v137, s[16:17] nt
	global_load_dwordx4 v[72:75], v138, s[16:17] nt
	global_load_dwordx4 v[76:79], v139, s[16:17] nt
	s_add_u32 s16, s16, 0x4000
	s_addc_u32 s17, s17, 0
	s_nop 0
	global_load_dwordx4 v[80:83], v136, s[16:17] nt
	global_load_dwordx4 v[84:87], v137, s[16:17] nt
	global_load_dwordx4 v[88:91], v138, s[16:17] nt
	global_load_dwordx4 v[92:95], v139, s[16:17] nt
	s_add_u32 s16, s16, 0x4000
	s_addc_u32 s17, s17, 0
	s_nop 0
	global_load_dwordx4 v[96:99], v136, s[16:17] nt
	global_load_dwordx4 v[100:103], v137, s[16:17] nt
	global_load_dwordx4 v[104:107], v138, s[16:17] nt
	global_load_dwordx4 v[108:111], v139, s[16:17] nt
	s_add_u32 s16, s16, 0x4000
	s_addc_u32 s17, s17, 0
	s_nop 0
	global_load_dwordx4 v[112:115], v136, s[16:17] nt
	global_load_dwordx4 v[116:119], v137, s[16:17] nt
	global_load_dwordx4 v[120:123], v138, s[16:17] nt
	global_load_dwordx4 v[124:127], v139, s[16:17] nt
	s_waitcnt vmcnt(16)
	s_branch .Lp2c0_p_st

.Lp2c0_p_st:
	s_lshr_b32 s22, s4, 8
	s_and_b32 s23, s4, 0xff
	s_and_b32 s27, s22, 1
	s_lshr_b32 s22, s22, 1
	s_add_i32 s22, s22, 20
	s_mul_i32 s24, s22, 0x300000
	s_lshr_b32 s25, s23, 5
	s_lshl_b32 s25, s25, 7
	s_add_i32 s24, s24, s25
	s_and_b32 s26, s23, 31
	s_lshr_b32 s25, s26, 2
	s_lshl_b32 s25, s25, 18
	s_add_i32 s24, s24, s25
	s_lshl_b32 s25, s27, 17
	s_add_i32 s24, s24, s25
	s_and_b32 s25, s26, 3
	s_lshl_b32 s25, s25, 15
	s_add_i32 s24, s24, s25
	s_add_u32 s20, s10, s24
	s_addc_u32 s21, s11, 0
	v_mul_f32_e32 v0, 0x42000000, v0
	v_mul_f32_e32 v4, 0x42000000, v4
	v_mul_f32_e32 v8, 0x42000000, v8
	v_mul_f32_e32 v12, 0x42000000, v12
	v_mul_f32_e32 v16, 0x42000000, v16
	v_mul_f32_e32 v20, 0x42000000, v20
	v_mul_f32_e32 v24, 0x42000000, v24
	v_mul_f32_e32 v28, 0x42000000, v28
	v_mul_f32_e32 v32, 0x42000000, v32
	v_mul_f32_e32 v36, 0x42000000, v36
	v_mul_f32_e32 v40, 0x42000000, v40
	v_mul_f32_e32 v44, 0x42000000, v44
	v_mul_f32_e32 v48, 0x42000000, v48
	v_mul_f32_e32 v52, 0x42000000, v52
	v_mul_f32_e32 v56, 0x42000000, v56
	v_mul_f32_e32 v60, 0x42000000, v60
	v_med3_f32 v0, v0, s28, v141
	v_med3_f32 v4, v4, s28, v141
	v_med3_f32 v8, v8, s28, v141
	v_med3_f32 v12, v12, s28, v141
	v_med3_f32 v16, v16, s28, v141
	v_med3_f32 v20, v20, s28, v141
	v_med3_f32 v24, v24, s28, v141
	v_med3_f32 v28, v28, s28, v141
	v_med3_f32 v32, v32, s28, v141
	v_med3_f32 v36, v36, s28, v141
	v_med3_f32 v40, v40, s28, v141
	v_med3_f32 v44, v44, s28, v141
	v_med3_f32 v48, v48, s28, v141
	v_med3_f32 v52, v52, s28, v141
	v_med3_f32 v56, v56, s28, v141
	v_med3_f32 v60, v60, s28, v141
	v_cvt_pk_fp8_f32 v128, v0, v4
	v_cvt_pk_fp8_f32 v129, v16, v20
	v_cvt_pk_fp8_f32 v130, v32, v36
	v_cvt_pk_fp8_f32 v131, v48, v52
	v_cvt_pk_fp8_f32 v128, v8, v12 op_sel:[0,0,1]
	v_cvt_pk_fp8_f32 v129, v24, v28 op_sel:[0,0,1]
	v_cvt_pk_fp8_f32 v130, v40, v44 op_sel:[0,0,1]
	v_cvt_pk_fp8_f32 v131, v56, v60 op_sel:[0,0,1]
	s_nop 0
	global_store_dwordx4 v140, v[128:131], s[20:21]
	v_mul_f32_e32 v1, 0x42000000, v1
	v_mul_f32_e32 v5, 0x42000000, v5
	v_mul_f32_e32 v9, 0x42000000, v9
	v_mul_f32_e32 v13, 0x42000000, v13
	v_mul_f32_e32 v17, 0x42000000, v17
	v_mul_f32_e32 v21, 0x42000000, v21
	v_mul_f32_e32 v25, 0x42000000, v25
	v_mul_f32_e32 v29, 0x42000000, v29
	v_mul_f32_e32 v33, 0x42000000, v33
	v_mul_f32_e32 v37, 0x42000000, v37
	v_mul_f32_e32 v41, 0x42000000, v41
	v_mul_f32_e32 v45, 0x42000000, v45
	v_mul_f32_e32 v49, 0x42000000, v49
	v_mul_f32_e32 v53, 0x42000000, v53
	v_mul_f32_e32 v57, 0x42000000, v57
	v_mul_f32_e32 v61, 0x42000000, v61
	v_med3_f32 v1, v1, s28, v141
	v_med3_f32 v5, v5, s28, v141
	v_med3_f32 v9, v9, s28, v141
	v_med3_f32 v13, v13, s28, v141
	v_med3_f32 v17, v17, s28, v141
	v_med3_f32 v21, v21, s28, v141
	v_med3_f32 v25, v25, s28, v141
	v_med3_f32 v29, v29, s28, v141
	v_med3_f32 v33, v33, s28, v141
	v_med3_f32 v37, v37, s28, v141
	v_med3_f32 v41, v41, s28, v141
	v_med3_f32 v45, v45, s28, v141
	v_med3_f32 v49, v49, s28, v141
	v_med3_f32 v53, v53, s28, v141
	v_med3_f32 v57, v57, s28, v141
	v_med3_f32 v61, v61, s28, v141
	v_cvt_pk_fp8_f32 v132, v1, v5
	v_cvt_pk_fp8_f32 v133, v17, v21
	v_cvt_pk_fp8_f32 v134, v33, v37
	v_cvt_pk_fp8_f32 v135, v49, v53
	v_cvt_pk_fp8_f32 v132, v9, v13 op_sel:[0,0,1]
	v_cvt_pk_fp8_f32 v133, v25, v29 op_sel:[0,0,1]
	v_cvt_pk_fp8_f32 v134, v41, v45 op_sel:[0,0,1]
	v_cvt_pk_fp8_f32 v135, v57, v61 op_sel:[0,0,1]
	s_nop 0
	global_store_dwordx4 v140, v[132:135], s[20:21] offset:1024
	v_mul_f32_e32 v2, 0x42000000, v2
	v_mul_f32_e32 v6, 0x42000000, v6
	v_mul_f32_e32 v10, 0x42000000, v10
	v_mul_f32_e32 v14, 0x42000000, v14
	v_mul_f32_e32 v18, 0x42000000, v18
	v_mul_f32_e32 v22, 0x42000000, v22
	v_mul_f32_e32 v26, 0x42000000, v26
	v_mul_f32_e32 v30, 0x42000000, v30
	v_mul_f32_e32 v34, 0x42000000, v34
	v_mul_f32_e32 v38, 0x42000000, v38
	v_mul_f32_e32 v42, 0x42000000, v42
	v_mul_f32_e32 v46, 0x42000000, v46
	v_mul_f32_e32 v50, 0x42000000, v50
	v_mul_f32_e32 v54, 0x42000000, v54
	v_mul_f32_e32 v58, 0x42000000, v58
	v_mul_f32_e32 v62, 0x42000000, v62
	v_med3_f32 v2, v2, s28, v141
	v_med3_f32 v6, v6, s28, v141
	v_med3_f32 v10, v10, s28, v141
	v_med3_f32 v14, v14, s28, v141
	v_med3_f32 v18, v18, s28, v141
	v_med3_f32 v22, v22, s28, v141
	v_med3_f32 v26, v26, s28, v141
	v_med3_f32 v30, v30, s28, v141
	v_med3_f32 v34, v34, s28, v141
	v_med3_f32 v38, v38, s28, v141
	v_med3_f32 v42, v42, s28, v141
	v_med3_f32 v46, v46, s28, v141
	v_med3_f32 v50, v50, s28, v141
	v_med3_f32 v54, v54, s28, v141
	v_med3_f32 v58, v58, s28, v141
	v_med3_f32 v62, v62, s28, v141
	v_cvt_pk_fp8_f32 v128, v2, v6
	v_cvt_pk_fp8_f32 v129, v18, v22
	v_cvt_pk_fp8_f32 v130, v34, v38
	v_cvt_pk_fp8_f32 v131, v50, v54
	v_cvt_pk_fp8_f32 v128, v10, v14 op_sel:[0,0,1]
	v_cvt_pk_fp8_f32 v129, v26, v30 op_sel:[0,0,1]
	v_cvt_pk_fp8_f32 v130, v42, v46 op_sel:[0,0,1]
	v_cvt_pk_fp8_f32 v131, v58, v62 op_sel:[0,0,1]
	s_nop 0
	global_store_dwordx4 v140, v[128:131], s[20:21] offset:2048
	v_mul_f32_e32 v3, 0x42000000, v3
	v_mul_f32_e32 v7, 0x42000000, v7
	v_mul_f32_e32 v11, 0x42000000, v11
	v_mul_f32_e32 v15, 0x42000000, v15
	v_mul_f32_e32 v19, 0x42000000, v19
	v_mul_f32_e32 v23, 0x42000000, v23
	v_mul_f32_e32 v27, 0x42000000, v27
	v_mul_f32_e32 v31, 0x42000000, v31
	v_mul_f32_e32 v35, 0x42000000, v35
	v_mul_f32_e32 v39, 0x42000000, v39
	v_mul_f32_e32 v43, 0x42000000, v43
	v_mul_f32_e32 v47, 0x42000000, v47
	v_mul_f32_e32 v51, 0x42000000, v51
	v_mul_f32_e32 v55, 0x42000000, v55
	v_mul_f32_e32 v59, 0x42000000, v59
	v_mul_f32_e32 v63, 0x42000000, v63
	v_med3_f32 v3, v3, s28, v141
	v_med3_f32 v7, v7, s28, v141
	v_med3_f32 v11, v11, s28, v141
	v_med3_f32 v15, v15, s28, v141
	v_med3_f32 v19, v19, s28, v141
	v_med3_f32 v23, v23, s28, v141
	v_med3_f32 v27, v27, s28, v141
	v_med3_f32 v31, v31, s28, v141
	v_med3_f32 v35, v35, s28, v141
	v_med3_f32 v39, v39, s28, v141
	v_med3_f32 v43, v43, s28, v141
	v_med3_f32 v47, v47, s28, v141
	v_med3_f32 v51, v51, s28, v141
	v_med3_f32 v55, v55, s28, v141
	v_med3_f32 v59, v59, s28, v141
	v_med3_f32 v63, v63, s28, v141
	v_cvt_pk_fp8_f32 v132, v3, v7
	v_cvt_pk_fp8_f32 v133, v19, v23
	v_cvt_pk_fp8_f32 v134, v35, v39
	v_cvt_pk_fp8_f32 v135, v51, v55
	v_cvt_pk_fp8_f32 v132, v11, v15 op_sel:[0,0,1]
	v_cvt_pk_fp8_f32 v133, v27, v31 op_sel:[0,0,1]
	v_cvt_pk_fp8_f32 v134, v43, v47 op_sel:[0,0,1]
	v_cvt_pk_fp8_f32 v135, v59, v63 op_sel:[0,0,1]
	s_nop 0
	global_store_dwordx4 v140, v[132:135], s[20:21] offset:3072
	s_cmp_ge_u32 s7, s6
	s_cbranch_scc1 .Lp2c0_done
	s_mov_b32 s4, s7
.Lp2c0_loop:
	s_add_i32 s7, s4, s5
	s_cmp_lt_u32 s7, s6
	s_cbranch_scc0 .Lp2c0_B_last
	s_lshr_b32 s22, s7, 8
	s_and_b32 s23, s7, 0xff
	s_and_b32 s27, s22, 1
	s_lshr_b32 s22, s22, 1
	s_cmp_eq_u32 s27, 0
	s_cselect_b64 s[16:17], s[12:13], s[14:15]
	s_add_i32 s22, s22, 20
	s_lshl_b32 s24, s22, 22
	s_lshr_b32 s25, s23, 5
	s_lshl_b32 s25, s25, 19
	s_and_b32 s26, s23, 31
	s_lshl_b32 s26, s26, 7
	s_add_i32 s24, s24, s25
	s_add_i32 s24, s24, s26
	s_add_u32 s16, s16, s24
	s_addc_u32 s17, s17, 0
	s_nop 0
	global_load_dwordx4 v[0:3], v136, s[16:17] nt
	global_load_dwordx4 v[4:7], v137, s[16:17] nt
	global_load_dwordx4 v[8:11], v138, s[16:17] nt
	global_load_dwordx4 v[12:15], v139, s[16:17] nt
	s_add_u32 s16, s16, 0x4000
	s_addc_u32 s17, s17, 0
	s_nop 0
	global_load_dwordx4 v[16:19], v136, s[16:17] nt
	global_load_dwordx4 v[20:23], v137, s[16:17] nt
	global_load_dwordx4 v[24:27], v138, s[16:17] nt
	global_load_dwordx4 v[28:31], v139, s[16:17] nt
	s_add_u32 s16, s16, 0x4000
	s_addc_u32 s17, s17, 0
	s_nop 0
	global_load_dwordx4 v[32:35], v136, s[16:17] nt
	global_load_dwordx4 v[36:39], v137, s[16:17] nt
	global_load_dwordx4 v[40:43], v138, s[16:17] nt
	global_load_dwordx4 v[44:47], v139, s[16:17] nt
	s_add_u32 s16, s16, 0x4000
	s_addc_u32 s17, s17, 0
	s_nop 0
	global_load_dwordx4 v[48:51], v136, s[16:17] nt
	global_load_dwordx4 v[52:55], v137, s[16:17] nt
	global_load_dwordx4 v[56:59], v138, s[16:17] nt
	global_load_dwordx4 v[60:63], v139, s[16:17] nt
	s_waitcnt vmcnt(20)
	s_branch .Lp2c0_B_st

.Lp2c0_B_st:
	s_lshr_b32 s22, s4, 8
	s_and_b32 s23, s4, 0xff
	s_and_b32 s27, s22, 1
	s_lshr_b32 s22, s22, 1
	s_add_i32 s22, s22, 20
	s_mul_i32 s24, s22, 0x300000
	s_lshr_b32 s25, s23, 5
	s_lshl_b32 s25, s25, 7
	s_add_i32 s24, s24, s25
	s_and_b32 s26, s23, 31
	s_lshr_b32 s25, s26, 2
	s_lshl_b32 s25, s25, 18
	s_add_i32 s24, s24, s25
	s_lshl_b32 s25, s27, 17
	s_add_i32 s24, s24, s25
	s_and_b32 s25, s26, 3
	s_lshl_b32 s25, s25, 15
	s_add_i32 s24, s24, s25
	s_add_u32 s20, s10, s24
	s_addc_u32 s21, s11, 0
	v_mul_f32_e32 v64, 0x42000000, v64
	v_mul_f32_e32 v68, 0x42000000, v68
	v_mul_f32_e32 v72, 0x42000000, v72
	v_mul_f32_e32 v76, 0x42000000, v76
	v_mul_f32_e32 v80, 0x42000000, v80
	v_mul_f32_e32 v84, 0x42000000, v84
	v_mul_f32_e32 v88, 0x42000000, v88
	v_mul_f32_e32 v92, 0x42000000, v92
	v_mul_f32_e32 v96, 0x42000000, v96
	v_mul_f32_e32 v100, 0x42000000, v100
	v_mul_f32_e32 v104, 0x42000000, v104
	v_mul_f32_e32 v108, 0x42000000, v108
	v_mul_f32_e32 v112, 0x42000000, v112
	v_mul_f32_e32 v116, 0x42000000, v116
	v_mul_f32_e32 v120, 0x42000000, v120
	v_mul_f32_e32 v124, 0x42000000, v124
	v_med3_f32 v64, v64, s28, v141
	v_med3_f32 v68, v68, s28, v141
	v_med3_f32 v72, v72, s28, v141
	v_med3_f32 v76, v76, s28, v141
	v_med3_f32 v80, v80, s28, v141
	v_med3_f32 v84, v84, s28, v141
	v_med3_f32 v88, v88, s28, v141
	v_med3_f32 v92, v92, s28, v141
	v_med3_f32 v96, v96, s28, v141
	v_med3_f32 v100, v100, s28, v141
	v_med3_f32 v104, v104, s28, v141
	v_med3_f32 v108, v108, s28, v141
	v_med3_f32 v112, v112, s28, v141
	v_med3_f32 v116, v116, s28, v141
	v_med3_f32 v120, v120, s28, v141
	v_med3_f32 v124, v124, s28, v141
	v_cvt_pk_fp8_f32 v128, v64, v68
	v_cvt_pk_fp8_f32 v129, v80, v84
	v_cvt_pk_fp8_f32 v130, v96, v100
	v_cvt_pk_fp8_f32 v131, v112, v116
	v_cvt_pk_fp8_f32 v128, v72, v76 op_sel:[0,0,1]
	v_cvt_pk_fp8_f32 v129, v88, v92 op_sel:[0,0,1]
	v_cvt_pk_fp8_f32 v130, v104, v108 op_sel:[0,0,1]
	v_cvt_pk_fp8_f32 v131, v120, v124 op_sel:[0,0,1]
	s_nop 0
	global_store_dwordx4 v140, v[128:131], s[20:21]
	v_mul_f32_e32 v65, 0x42000000, v65
	v_mul_f32_e32 v69, 0x42000000, v69
	v_mul_f32_e32 v73, 0x42000000, v73
	v_mul_f32_e32 v77, 0x42000000, v77
	v_mul_f32_e32 v81, 0x42000000, v81
	v_mul_f32_e32 v85, 0x42000000, v85
	v_mul_f32_e32 v89, 0x42000000, v89
	v_mul_f32_e32 v93, 0x42000000, v93
	v_mul_f32_e32 v97, 0x42000000, v97
	v_mul_f32_e32 v101, 0x42000000, v101
	v_mul_f32_e32 v105, 0x42000000, v105
	v_mul_f32_e32 v109, 0x42000000, v109
	v_mul_f32_e32 v113, 0x42000000, v113
	v_mul_f32_e32 v117, 0x42000000, v117
	v_mul_f32_e32 v121, 0x42000000, v121
	v_mul_f32_e32 v125, 0x42000000, v125
	v_med3_f32 v65, v65, s28, v141
	v_med3_f32 v69, v69, s28, v141
	v_med3_f32 v73, v73, s28, v141
	v_med3_f32 v77, v77, s28, v141
	v_med3_f32 v81, v81, s28, v141
	v_med3_f32 v85, v85, s28, v141
	v_med3_f32 v89, v89, s28, v141
	v_med3_f32 v93, v93, s28, v141
	v_med3_f32 v97, v97, s28, v141
	v_med3_f32 v101, v101, s28, v141
	v_med3_f32 v105, v105, s28, v141
	v_med3_f32 v109, v109, s28, v141
	v_med3_f32 v113, v113, s28, v141
	v_med3_f32 v117, v117, s28, v141
	v_med3_f32 v121, v121, s28, v141
	v_med3_f32 v125, v125, s28, v141
	v_cvt_pk_fp8_f32 v132, v65, v69
	v_cvt_pk_fp8_f32 v133, v81, v85
	v_cvt_pk_fp8_f32 v134, v97, v101
	v_cvt_pk_fp8_f32 v135, v113, v117
	v_cvt_pk_fp8_f32 v132, v73, v77 op_sel:[0,0,1]
	v_cvt_pk_fp8_f32 v133, v89, v93 op_sel:[0,0,1]
	v_cvt_pk_fp8_f32 v134, v105, v109 op_sel:[0,0,1]
	v_cvt_pk_fp8_f32 v135, v121, v125 op_sel:[0,0,1]
	s_nop 0
	global_store_dwordx4 v140, v[132:135], s[20:21] offset:1024
	v_mul_f32_e32 v66, 0x42000000, v66
	v_mul_f32_e32 v70, 0x42000000, v70
	v_mul_f32_e32 v74, 0x42000000, v74
	v_mul_f32_e32 v78, 0x42000000, v78
	v_mul_f32_e32 v82, 0x42000000, v82
	v_mul_f32_e32 v86, 0x42000000, v86
	v_mul_f32_e32 v90, 0x42000000, v90
	v_mul_f32_e32 v94, 0x42000000, v94
	v_mul_f32_e32 v98, 0x42000000, v98
	v_mul_f32_e32 v102, 0x42000000, v102
	v_mul_f32_e32 v106, 0x42000000, v106
	v_mul_f32_e32 v110, 0x42000000, v110
	v_mul_f32_e32 v114, 0x42000000, v114
	v_mul_f32_e32 v118, 0x42000000, v118
	v_mul_f32_e32 v122, 0x42000000, v122
	v_mul_f32_e32 v126, 0x42000000, v126
	v_med3_f32 v66, v66, s28, v141
	v_med3_f32 v70, v70, s28, v141
	v_med3_f32 v74, v74, s28, v141
	v_med3_f32 v78, v78, s28, v141
	v_med3_f32 v82, v82, s28, v141
	v_med3_f32 v86, v86, s28, v141
	v_med3_f32 v90, v90, s28, v141
	v_med3_f32 v94, v94, s28, v141
	v_med3_f32 v98, v98, s28, v141
	v_med3_f32 v102, v102, s28, v141
	v_med3_f32 v106, v106, s28, v141
	v_med3_f32 v110, v110, s28, v141
	v_med3_f32 v114, v114, s28, v141
	v_med3_f32 v118, v118, s28, v141
	v_med3_f32 v122, v122, s28, v141
	v_med3_f32 v126, v126, s28, v141
	v_cvt_pk_fp8_f32 v128, v66, v70
	v_cvt_pk_fp8_f32 v129, v82, v86
	v_cvt_pk_fp8_f32 v130, v98, v102
	v_cvt_pk_fp8_f32 v131, v114, v118
	v_cvt_pk_fp8_f32 v128, v74, v78 op_sel:[0,0,1]
	v_cvt_pk_fp8_f32 v129, v90, v94 op_sel:[0,0,1]
	v_cvt_pk_fp8_f32 v130, v106, v110 op_sel:[0,0,1]
	v_cvt_pk_fp8_f32 v131, v122, v126 op_sel:[0,0,1]
	s_nop 0
	global_store_dwordx4 v140, v[128:131], s[20:21] offset:2048
	v_mul_f32_e32 v67, 0x42000000, v67
	v_mul_f32_e32 v71, 0x42000000, v71
	v_mul_f32_e32 v75, 0x42000000, v75
	v_mul_f32_e32 v79, 0x42000000, v79
	v_mul_f32_e32 v83, 0x42000000, v83
	v_mul_f32_e32 v87, 0x42000000, v87
	v_mul_f32_e32 v91, 0x42000000, v91
	v_mul_f32_e32 v95, 0x42000000, v95
	v_mul_f32_e32 v99, 0x42000000, v99
	v_mul_f32_e32 v103, 0x42000000, v103
	v_mul_f32_e32 v107, 0x42000000, v107
	v_mul_f32_e32 v111, 0x42000000, v111
	v_mul_f32_e32 v115, 0x42000000, v115
	v_mul_f32_e32 v119, 0x42000000, v119
	v_mul_f32_e32 v123, 0x42000000, v123
	v_mul_f32_e32 v127, 0x42000000, v127
	v_med3_f32 v67, v67, s28, v141
	v_med3_f32 v71, v71, s28, v141
	v_med3_f32 v75, v75, s28, v141
	v_med3_f32 v79, v79, s28, v141
	v_med3_f32 v83, v83, s28, v141
	v_med3_f32 v87, v87, s28, v141
	v_med3_f32 v91, v91, s28, v141
	v_med3_f32 v95, v95, s28, v141
	v_med3_f32 v99, v99, s28, v141
	v_med3_f32 v103, v103, s28, v141
	v_med3_f32 v107, v107, s28, v141
	v_med3_f32 v111, v111, s28, v141
	v_med3_f32 v115, v115, s28, v141
	v_med3_f32 v119, v119, s28, v141
	v_med3_f32 v123, v123, s28, v141
	v_med3_f32 v127, v127, s28, v141
	v_cvt_pk_fp8_f32 v132, v67, v71
	v_cvt_pk_fp8_f32 v133, v83, v87
	v_cvt_pk_fp8_f32 v134, v99, v103
	v_cvt_pk_fp8_f32 v135, v115, v119
	v_cvt_pk_fp8_f32 v132, v75, v79 op_sel:[0,0,1]
	v_cvt_pk_fp8_f32 v133, v91, v95 op_sel:[0,0,1]
	v_cvt_pk_fp8_f32 v134, v107, v111 op_sel:[0,0,1]
	v_cvt_pk_fp8_f32 v135, v123, v127 op_sel:[0,0,1]
	s_nop 0
	global_store_dwordx4 v140, v[132:135], s[20:21] offset:3072
	s_cmp_ge_u32 s7, s6
	s_cbranch_scc1 .Lp2c0_done
	s_mov_b32 s4, s7
	s_add_i32 s7, s4, s5
	s_cmp_lt_u32 s7, s6
	s_cbranch_scc0 .Lp2c0_A_last
	s_lshr_b32 s22, s7, 8
	s_and_b32 s23, s7, 0xff
	s_and_b32 s27, s22, 1
	s_lshr_b32 s22, s22, 1
	s_cmp_eq_u32 s27, 0
	s_cselect_b64 s[16:17], s[12:13], s[14:15]
	s_add_i32 s22, s22, 20
	s_lshl_b32 s24, s22, 22
	s_lshr_b32 s25, s23, 5
	s_lshl_b32 s25, s25, 19
	s_and_b32 s26, s23, 31
	s_lshl_b32 s26, s26, 7
	s_add_i32 s24, s24, s25
	s_add_i32 s24, s24, s26
	s_add_u32 s16, s16, s24
	s_addc_u32 s17, s17, 0
	s_nop 0
	global_load_dwordx4 v[64:67], v136, s[16:17] nt
	global_load_dwordx4 v[68:71], v137, s[16:17] nt
	global_load_dwordx4 v[72:75], v138, s[16:17] nt
	global_load_dwordx4 v[76:79], v139, s[16:17] nt
	s_add_u32 s16, s16, 0x4000
	s_addc_u32 s17, s17, 0
	s_nop 0
	global_load_dwordx4 v[80:83], v136, s[16:17] nt
	global_load_dwordx4 v[84:87], v137, s[16:17] nt
	global_load_dwordx4 v[88:91], v138, s[16:17] nt
	global_load_dwordx4 v[92:95], v139, s[16:17] nt
	s_add_u32 s16, s16, 0x4000
	s_addc_u32 s17, s17, 0
	s_nop 0
	global_load_dwordx4 v[96:99], v136, s[16:17] nt
	global_load_dwordx4 v[100:103], v137, s[16:17] nt
	global_load_dwordx4 v[104:107], v138, s[16:17] nt
	global_load_dwordx4 v[108:111], v139, s[16:17] nt
	s_add_u32 s16, s16, 0x4000
	s_addc_u32 s17, s17, 0
	s_nop 0
	global_load_dwordx4 v[112:115], v136, s[16:17] nt
	global_load_dwordx4 v[116:119], v137, s[16:17] nt
	global_load_dwordx4 v[120:123], v138, s[16:17] nt
	global_load_dwordx4 v[124:127], v139, s[16:17] nt
	s_waitcnt vmcnt(20)
	s_branch .Lp2c0_A_st

.Lp2c0_A_st:
	s_lshr_b32 s22, s4, 8
	s_and_b32 s23, s4, 0xff
	s_and_b32 s27, s22, 1
	s_lshr_b32 s22, s22, 1
	s_add_i32 s22, s22, 20
	s_mul_i32 s24, s22, 0x300000
	s_lshr_b32 s25, s23, 5
	s_lshl_b32 s25, s25, 7
	s_add_i32 s24, s24, s25
	s_and_b32 s26, s23, 31
	s_lshr_b32 s25, s26, 2
	s_lshl_b32 s25, s25, 18
	s_add_i32 s24, s24, s25
	s_lshl_b32 s25, s27, 17
	s_add_i32 s24, s24, s25
	s_and_b32 s25, s26, 3
	s_lshl_b32 s25, s25, 15
	s_add_i32 s24, s24, s25
	s_add_u32 s20, s10, s24
	s_addc_u32 s21, s11, 0
	v_mul_f32_e32 v0, 0x42000000, v0
	v_mul_f32_e32 v4, 0x42000000, v4
	v_mul_f32_e32 v8, 0x42000000, v8
	v_mul_f32_e32 v12, 0x42000000, v12
	v_mul_f32_e32 v16, 0x42000000, v16
	v_mul_f32_e32 v20, 0x42000000, v20
	v_mul_f32_e32 v24, 0x42000000, v24
	v_mul_f32_e32 v28, 0x42000000, v28
	v_mul_f32_e32 v32, 0x42000000, v32
	v_mul_f32_e32 v36, 0x42000000, v36
	v_mul_f32_e32 v40, 0x42000000, v40
	v_mul_f32_e32 v44, 0x42000000, v44
	v_mul_f32_e32 v48, 0x42000000, v48
	v_mul_f32_e32 v52, 0x42000000, v52
	v_mul_f32_e32 v56, 0x42000000, v56
	v_mul_f32_e32 v60, 0x42000000, v60
	v_med3_f32 v0, v0, s28, v141
	v_med3_f32 v4, v4, s28, v141
	v_med3_f32 v8, v8, s28, v141
	v_med3_f32 v12, v12, s28, v141
	v_med3_f32 v16, v16, s28, v141
	v_med3_f32 v20, v20, s28, v141
	v_med3_f32 v24, v24, s28, v141
	v_med3_f32 v28, v28, s28, v141
	v_med3_f32 v32, v32, s28, v141
	v_med3_f32 v36, v36, s28, v141
	v_med3_f32 v40, v40, s28, v141
	v_med3_f32 v44, v44, s28, v141
	v_med3_f32 v48, v48, s28, v141
	v_med3_f32 v52, v52, s28, v141
	v_med3_f32 v56, v56, s28, v141
	v_med3_f32 v60, v60, s28, v141
	v_cvt_pk_fp8_f32 v128, v0, v4
	v_cvt_pk_fp8_f32 v129, v16, v20
	v_cvt_pk_fp8_f32 v130, v32, v36
	v_cvt_pk_fp8_f32 v131, v48, v52
	v_cvt_pk_fp8_f32 v128, v8, v12 op_sel:[0,0,1]
	v_cvt_pk_fp8_f32 v129, v24, v28 op_sel:[0,0,1]
	v_cvt_pk_fp8_f32 v130, v40, v44 op_sel:[0,0,1]
	v_cvt_pk_fp8_f32 v131, v56, v60 op_sel:[0,0,1]
	s_nop 0
	global_store_dwordx4 v140, v[128:131], s[20:21]
	v_mul_f32_e32 v1, 0x42000000, v1
	v_mul_f32_e32 v5, 0x42000000, v5
	v_mul_f32_e32 v9, 0x42000000, v9
	v_mul_f32_e32 v13, 0x42000000, v13
	v_mul_f32_e32 v17, 0x42000000, v17
	v_mul_f32_e32 v21, 0x42000000, v21
	v_mul_f32_e32 v25, 0x42000000, v25
	v_mul_f32_e32 v29, 0x42000000, v29
	v_mul_f32_e32 v33, 0x42000000, v33
	v_mul_f32_e32 v37, 0x42000000, v37
	v_mul_f32_e32 v41, 0x42000000, v41
	v_mul_f32_e32 v45, 0x42000000, v45
	v_mul_f32_e32 v49, 0x42000000, v49
	v_mul_f32_e32 v53, 0x42000000, v53
	v_mul_f32_e32 v57, 0x42000000, v57
	v_mul_f32_e32 v61, 0x42000000, v61
	v_med3_f32 v1, v1, s28, v141
	v_med3_f32 v5, v5, s28, v141
	v_med3_f32 v9, v9, s28, v141
	v_med3_f32 v13, v13, s28, v141
	v_med3_f32 v17, v17, s28, v141
	v_med3_f32 v21, v21, s28, v141
	v_med3_f32 v25, v25, s28, v141
	v_med3_f32 v29, v29, s28, v141
	v_med3_f32 v33, v33, s28, v141
	v_med3_f32 v37, v37, s28, v141
	v_med3_f32 v41, v41, s28, v141
	v_med3_f32 v45, v45, s28, v141
	v_med3_f32 v49, v49, s28, v141
	v_med3_f32 v53, v53, s28, v141
	v_med3_f32 v57, v57, s28, v141
	v_med3_f32 v61, v61, s28, v141
	v_cvt_pk_fp8_f32 v132, v1, v5
	v_cvt_pk_fp8_f32 v133, v17, v21
	v_cvt_pk_fp8_f32 v134, v33, v37
	v_cvt_pk_fp8_f32 v135, v49, v53
	v_cvt_pk_fp8_f32 v132, v9, v13 op_sel:[0,0,1]
	v_cvt_pk_fp8_f32 v133, v25, v29 op_sel:[0,0,1]
	v_cvt_pk_fp8_f32 v134, v41, v45 op_sel:[0,0,1]
	v_cvt_pk_fp8_f32 v135, v57, v61 op_sel:[0,0,1]
	s_nop 0
	global_store_dwordx4 v140, v[132:135], s[20:21] offset:1024
	v_mul_f32_e32 v2, 0x42000000, v2
	v_mul_f32_e32 v6, 0x42000000, v6
	v_mul_f32_e32 v10, 0x42000000, v10
	v_mul_f32_e32 v14, 0x42000000, v14
	v_mul_f32_e32 v18, 0x42000000, v18
	v_mul_f32_e32 v22, 0x42000000, v22
	v_mul_f32_e32 v26, 0x42000000, v26
	v_mul_f32_e32 v30, 0x42000000, v30
	v_mul_f32_e32 v34, 0x42000000, v34
	v_mul_f32_e32 v38, 0x42000000, v38
	v_mul_f32_e32 v42, 0x42000000, v42
	v_mul_f32_e32 v46, 0x42000000, v46
	v_mul_f32_e32 v50, 0x42000000, v50
	v_mul_f32_e32 v54, 0x42000000, v54
	v_mul_f32_e32 v58, 0x42000000, v58
	v_mul_f32_e32 v62, 0x42000000, v62
	v_med3_f32 v2, v2, s28, v141
	v_med3_f32 v6, v6, s28, v141
	v_med3_f32 v10, v10, s28, v141
	v_med3_f32 v14, v14, s28, v141
	v_med3_f32 v18, v18, s28, v141
	v_med3_f32 v22, v22, s28, v141
	v_med3_f32 v26, v26, s28, v141
	v_med3_f32 v30, v30, s28, v141
	v_med3_f32 v34, v34, s28, v141
	v_med3_f32 v38, v38, s28, v141
	v_med3_f32 v42, v42, s28, v141
	v_med3_f32 v46, v46, s28, v141
	v_med3_f32 v50, v50, s28, v141
	v_med3_f32 v54, v54, s28, v141
	v_med3_f32 v58, v58, s28, v141
	v_med3_f32 v62, v62, s28, v141
	v_cvt_pk_fp8_f32 v128, v2, v6
	v_cvt_pk_fp8_f32 v129, v18, v22
	v_cvt_pk_fp8_f32 v130, v34, v38
	v_cvt_pk_fp8_f32 v131, v50, v54
	v_cvt_pk_fp8_f32 v128, v10, v14 op_sel:[0,0,1]
	v_cvt_pk_fp8_f32 v129, v26, v30 op_sel:[0,0,1]
	v_cvt_pk_fp8_f32 v130, v42, v46 op_sel:[0,0,1]
	v_cvt_pk_fp8_f32 v131, v58, v62 op_sel:[0,0,1]
	s_nop 0
	global_store_dwordx4 v140, v[128:131], s[20:21] offset:2048
	v_mul_f32_e32 v3, 0x42000000, v3
	v_mul_f32_e32 v7, 0x42000000, v7
	v_mul_f32_e32 v11, 0x42000000, v11
	v_mul_f32_e32 v15, 0x42000000, v15
	v_mul_f32_e32 v19, 0x42000000, v19
	v_mul_f32_e32 v23, 0x42000000, v23
	v_mul_f32_e32 v27, 0x42000000, v27
	v_mul_f32_e32 v31, 0x42000000, v31
	v_mul_f32_e32 v35, 0x42000000, v35
	v_mul_f32_e32 v39, 0x42000000, v39
	v_mul_f32_e32 v43, 0x42000000, v43
	v_mul_f32_e32 v47, 0x42000000, v47
	v_mul_f32_e32 v51, 0x42000000, v51
	v_mul_f32_e32 v55, 0x42000000, v55
	v_mul_f32_e32 v59, 0x42000000, v59
	v_mul_f32_e32 v63, 0x42000000, v63
	v_med3_f32 v3, v3, s28, v141
	v_med3_f32 v7, v7, s28, v141
	v_med3_f32 v11, v11, s28, v141
	v_med3_f32 v15, v15, s28, v141
	v_med3_f32 v19, v19, s28, v141
	v_med3_f32 v23, v23, s28, v141
	v_med3_f32 v27, v27, s28, v141
	v_med3_f32 v31, v31, s28, v141
	v_med3_f32 v35, v35, s28, v141
	v_med3_f32 v39, v39, s28, v141
	v_med3_f32 v43, v43, s28, v141
	v_med3_f32 v47, v47, s28, v141
	v_med3_f32 v51, v51, s28, v141
	v_med3_f32 v55, v55, s28, v141
	v_med3_f32 v59, v59, s28, v141
	v_med3_f32 v63, v63, s28, v141
	v_cvt_pk_fp8_f32 v132, v3, v7
	v_cvt_pk_fp8_f32 v133, v19, v23
	v_cvt_pk_fp8_f32 v134, v35, v39
	v_cvt_pk_fp8_f32 v135, v51, v55
	v_cvt_pk_fp8_f32 v132, v11, v15 op_sel:[0,0,1]
	v_cvt_pk_fp8_f32 v133, v27, v31 op_sel:[0,0,1]
	v_cvt_pk_fp8_f32 v134, v43, v47 op_sel:[0,0,1]
	v_cvt_pk_fp8_f32 v135, v59, v63 op_sel:[0,0,1]
	s_nop 0
	global_store_dwordx4 v140, v[132:135], s[20:21] offset:3072
	s_cmp_ge_u32 s7, s6
	s_cbranch_scc1 .Lp2c0_done
	s_mov_b32 s4, s7
	s_branch .Lp2c0_loop
.Lp2c0_done:
	s_mov_b32 s4, s19
	s_mov_b32 s5, 0x1c0
	s_mov_b32 s6, 0x1000
	s_waitcnt vmcnt(0)
	s_cmp_ge_u32 s4, s6
	s_cbranch_scc1 .Lp2c1_done
	v_readlane_b32 s8, v243, 7
	v_readlane_b32 s9, v243, 8
	s_load_dwordx2 s[10:11], s[8:9], 0x130
	s_load_dwordx2 s[12:13], s[8:9], 0x118
	v_mbcnt_lo_u32_b32 v142, -1, 0
	v_mbcnt_hi_u32_b32 v142, -1, v142
	v_lshrrev_b32_e32 v143, 3, v142
	v_and_b32_e32 v142, 7, v142
	v_lshlrev_b32_e32 v136, 16, v143
	v_lshl_add_u32 v136, v142, 4, v136
	v_add_u32_e32 v137, 0x1000, v136
	v_add_u32_e32 v138, 0x2000, v136
	v_add_u32_e32 v139, 0x3000, v136
	v_bfe_u32 v140, v142, 1, 1
	v_lshlrev_b32_e32 v140, 17, v140
	v_lshrrev_b32_e32 v144, 2, v142
	v_lshl_add_u32 v140, v144, 13, v140
	v_and_b32_e32 v144, 1, v142
	v_lshl_add_u32 v140, v144, 12, v140
	v_lshl_add_u32 v140, v143, 4, v140
	v_mov_b32_e32 v141, 0x43e00000
	s_mov_b32 s28, 0xc3e00000
	s_waitcnt lgkmcnt(0)
	s_add_u32 s10, s10, 0x2b00000
	s_addc_u32 s11, s11, 0
	s_lshr_b32 s22, s4, 8
	s_and_b32 s23, s4, 0xff
	s_mov_b64 s[16:17], s[12:13]
	s_add_i32 s22, s22, 48
	s_lshl_b32 s24, s22, 22
	s_lshr_b32 s25, s23, 5
	s_lshl_b32 s25, s25, 19
	s_and_b32 s26, s23, 31
	s_lshl_b32 s26, s26, 7
	s_add_i32 s24, s24, s25
	s_add_i32 s24, s24, s26
	s_add_u32 s16, s16, s24
	s_addc_u32 s17, s17, 0
	s_nop 0
	global_load_dwordx4 v[0:3], v136, s[16:17] nt
	global_load_dwordx4 v[4:7], v137, s[16:17] nt
	global_load_dwordx4 v[8:11], v138, s[16:17] nt
	global_load_dwordx4 v[12:15], v139, s[16:17] nt
	s_add_u32 s16, s16, 0x4000
	s_addc_u32 s17, s17, 0
	s_nop 0
	global_load_dwordx4 v[16:19], v136, s[16:17] nt
	global_load_dwordx4 v[20:23], v137, s[16:17] nt
	global_load_dwordx4 v[24:27], v138, s[16:17] nt
	global_load_dwordx4 v[28:31], v139, s[16:17] nt
	s_add_u32 s16, s16, 0x4000
	s_addc_u32 s17, s17, 0
	s_nop 0
	global_load_dwordx4 v[32:35], v136, s[16:17] nt
	global_load_dwordx4 v[36:39], v137, s[16:17] nt
	global_load_dwordx4 v[40:43], v138, s[16:17] nt
	global_load_dwordx4 v[44:47], v139, s[16:17] nt
	s_add_u32 s16, s16, 0x4000
	s_addc_u32 s17, s17, 0
	s_nop 0
	global_load_dwordx4 v[48:51], v136, s[16:17] nt
	global_load_dwordx4 v[52:55], v137, s[16:17] nt
	global_load_dwordx4 v[56:59], v138, s[16:17] nt
	global_load_dwordx4 v[60:63], v139, s[16:17] nt
	s_add_i32 s7, s4, s5
	s_cmp_lt_u32 s7, s6
	s_cbranch_scc0 .Lp2c1_p_last
	s_lshr_b32 s22, s7, 8
	s_and_b32 s23, s7, 0xff
	s_mov_b64 s[16:17], s[12:13]
	s_add_i32 s22, s22, 48
	s_lshl_b32 s24, s22, 22
	s_lshr_b32 s25, s23, 5
	s_lshl_b32 s25, s25, 19
	s_and_b32 s26, s23, 31
	s_lshl_b32 s26, s26, 7
	s_add_i32 s24, s24, s25
	s_add_i32 s24, s24, s26
	s_add_u32 s16, s16, s24
	s_addc_u32 s17, s17, 0
	s_nop 0
	global_load_dwordx4 v[64:67], v136, s[16:17] nt
	global_load_dwordx4 v[68:71], v137, s[16:17] nt
	global_load_dwordx4 v[72:75], v138, s[16:17] nt
	global_load_dwordx4 v[76:79], v139, s[16:17] nt
	s_add_u32 s16, s16, 0x4000
	s_addc_u32 s17, s17, 0
	s_nop 0
	global_load_dwordx4 v[80:83], v136, s[16:17] nt
	global_load_dwordx4 v[84:87], v137, s[16:17] nt
	global_load_dwordx4 v[88:91], v138, s[16:17] nt
	global_load_dwordx4 v[92:95], v139, s[16:17] nt
	s_add_u32 s16, s16, 0x4000
	s_addc_u32 s17, s17, 0
	s_nop 0
	global_load_dwordx4 v[96:99], v136, s[16:17] nt
	global_load_dwordx4 v[100:103], v137, s[16:17] nt
	global_load_dwordx4 v[104:107], v138, s[16:17] nt
	global_load_dwordx4 v[108:111], v139, s[16:17] nt
	s_add_u32 s16, s16, 0x4000
	s_addc_u32 s17, s17, 0
	s_nop 0
	global_load_dwordx4 v[112:115], v136, s[16:17] nt
	global_load_dwordx4 v[116:119], v137, s[16:17] nt
	global_load_dwordx4 v[120:123], v138, s[16:17] nt
	global_load_dwordx4 v[124:127], v139, s[16:17] nt
	s_waitcnt vmcnt(16)
	s_branch .Lp2c1_p_st

.Lp2c1_p_st:
	s_lshr_b32 s22, s4, 8
	s_and_b32 s23, s4, 0xff
	s_add_i32 s22, s22, 48
	s_mul_i32 s24, s22, 0x300000
	s_lshr_b32 s25, s23, 5
	s_lshl_b32 s25, s25, 7
	s_add_i32 s24, s24, s25
	s_and_b32 s26, s23, 31
	s_lshr_b32 s25, s26, 3
	s_lshl_b32 s25, s25, 18
	s_add_i32 s24, s24, s25
	s_bfe_u32 s25, s26, 0x20001
	s_lshl_b32 s25, s25, 15
	s_add_i32 s24, s24, s25
	s_and_b32 s25, s26, 1
	s_lshl_b32 s25, s25, 14
	s_add_i32 s24, s24, s25
	s_add_u32 s20, s10, s24
	s_addc_u32 s21, s11, 0
	v_mul_f32_e32 v0, 0x42000000, v0
	v_mul_f32_e32 v4, 0x42000000, v4
	v_mul_f32_e32 v8, 0x42000000, v8
	v_mul_f32_e32 v12, 0x42000000, v12
	v_mul_f32_e32 v16, 0x42000000, v16
	v_mul_f32_e32 v20, 0x42000000, v20
	v_mul_f32_e32 v24, 0x42000000, v24
	v_mul_f32_e32 v28, 0x42000000, v28
	v_mul_f32_e32 v32, 0x42000000, v32
	v_mul_f32_e32 v36, 0x42000000, v36
	v_mul_f32_e32 v40, 0x42000000, v40
	v_mul_f32_e32 v44, 0x42000000, v44
	v_mul_f32_e32 v48, 0x42000000, v48
	v_mul_f32_e32 v52, 0x42000000, v52
	v_mul_f32_e32 v56, 0x42000000, v56
	v_mul_f32_e32 v60, 0x42000000, v60
	v_med3_f32 v0, v0, s28, v141
	v_med3_f32 v4, v4, s28, v141
	v_med3_f32 v8, v8, s28, v141
	v_med3_f32 v12, v12, s28, v141
	v_med3_f32 v16, v16, s28, v141
	v_med3_f32 v20, v20, s28, v141
	v_med3_f32 v24, v24, s28, v141
	v_med3_f32 v28, v28, s28, v141
	v_med3_f32 v32, v32, s28, v141
	v_med3_f32 v36, v36, s28, v141
	v_med3_f32 v40, v40, s28, v141
	v_med3_f32 v44, v44, s28, v141
	v_med3_f32 v48, v48, s28, v141
	v_med3_f32 v52, v52, s28, v141
	v_med3_f32 v56, v56, s28, v141
	v_med3_f32 v60, v60, s28, v141
	v_cvt_pk_fp8_f32 v128, v0, v4
	v_cvt_pk_fp8_f32 v129, v16, v20
	v_cvt_pk_fp8_f32 v130, v32, v36
	v_cvt_pk_fp8_f32 v131, v48, v52
	v_cvt_pk_fp8_f32 v128, v8, v12 op_sel:[0,0,1]
	v_cvt_pk_fp8_f32 v129, v24, v28 op_sel:[0,0,1]
	v_cvt_pk_fp8_f32 v130, v40, v44 op_sel:[0,0,1]
	v_cvt_pk_fp8_f32 v131, v56, v60 op_sel:[0,0,1]
	s_nop 0
	global_store_dwordx4 v140, v[128:131], s[20:21]
	v_mul_f32_e32 v1, 0x42000000, v1
	v_mul_f32_e32 v5, 0x42000000, v5
	v_mul_f32_e32 v9, 0x42000000, v9
	v_mul_f32_e32 v13, 0x42000000, v13
	v_mul_f32_e32 v17, 0x42000000, v17
	v_mul_f32_e32 v21, 0x42000000, v21
	v_mul_f32_e32 v25, 0x42000000, v25
	v_mul_f32_e32 v29, 0x42000000, v29
	v_mul_f32_e32 v33, 0x42000000, v33
	v_mul_f32_e32 v37, 0x42000000, v37
	v_mul_f32_e32 v41, 0x42000000, v41
	v_mul_f32_e32 v45, 0x42000000, v45
	v_mul_f32_e32 v49, 0x42000000, v49
	v_mul_f32_e32 v53, 0x42000000, v53
	v_mul_f32_e32 v57, 0x42000000, v57
	v_mul_f32_e32 v61, 0x42000000, v61
	v_med3_f32 v1, v1, s28, v141
	v_med3_f32 v5, v5, s28, v141
	v_med3_f32 v9, v9, s28, v141
	v_med3_f32 v13, v13, s28, v141
	v_med3_f32 v17, v17, s28, v141
	v_med3_f32 v21, v21, s28, v141
	v_med3_f32 v25, v25, s28, v141
	v_med3_f32 v29, v29, s28, v141
	v_med3_f32 v33, v33, s28, v141
	v_med3_f32 v37, v37, s28, v141
	v_med3_f32 v41, v41, s28, v141
	v_med3_f32 v45, v45, s28, v141
	v_med3_f32 v49, v49, s28, v141
	v_med3_f32 v53, v53, s28, v141
	v_med3_f32 v57, v57, s28, v141
	v_med3_f32 v61, v61, s28, v141
	v_cvt_pk_fp8_f32 v132, v1, v5
	v_cvt_pk_fp8_f32 v133, v17, v21
	v_cvt_pk_fp8_f32 v134, v33, v37
	v_cvt_pk_fp8_f32 v135, v49, v53
	v_cvt_pk_fp8_f32 v132, v9, v13 op_sel:[0,0,1]
	v_cvt_pk_fp8_f32 v133, v25, v29 op_sel:[0,0,1]
	v_cvt_pk_fp8_f32 v134, v41, v45 op_sel:[0,0,1]
	v_cvt_pk_fp8_f32 v135, v57, v61 op_sel:[0,0,1]
	s_nop 0
	global_store_dwordx4 v140, v[132:135], s[20:21] offset:1024
	v_mul_f32_e32 v2, 0x42000000, v2
	v_mul_f32_e32 v6, 0x42000000, v6
	v_mul_f32_e32 v10, 0x42000000, v10
	v_mul_f32_e32 v14, 0x42000000, v14
	v_mul_f32_e32 v18, 0x42000000, v18
	v_mul_f32_e32 v22, 0x42000000, v22
	v_mul_f32_e32 v26, 0x42000000, v26
	v_mul_f32_e32 v30, 0x42000000, v30
	v_mul_f32_e32 v34, 0x42000000, v34
	v_mul_f32_e32 v38, 0x42000000, v38
	v_mul_f32_e32 v42, 0x42000000, v42
	v_mul_f32_e32 v46, 0x42000000, v46
	v_mul_f32_e32 v50, 0x42000000, v50
	v_mul_f32_e32 v54, 0x42000000, v54
	v_mul_f32_e32 v58, 0x42000000, v58
	v_mul_f32_e32 v62, 0x42000000, v62
	v_med3_f32 v2, v2, s28, v141
	v_med3_f32 v6, v6, s28, v141
	v_med3_f32 v10, v10, s28, v141
	v_med3_f32 v14, v14, s28, v141
	v_med3_f32 v18, v18, s28, v141
	v_med3_f32 v22, v22, s28, v141
	v_med3_f32 v26, v26, s28, v141
	v_med3_f32 v30, v30, s28, v141
	v_med3_f32 v34, v34, s28, v141
	v_med3_f32 v38, v38, s28, v141
	v_med3_f32 v42, v42, s28, v141
	v_med3_f32 v46, v46, s28, v141
	v_med3_f32 v50, v50, s28, v141
	v_med3_f32 v54, v54, s28, v141
	v_med3_f32 v58, v58, s28, v141
	v_med3_f32 v62, v62, s28, v141
	v_cvt_pk_fp8_f32 v128, v2, v6
	v_cvt_pk_fp8_f32 v129, v18, v22
	v_cvt_pk_fp8_f32 v130, v34, v38
	v_cvt_pk_fp8_f32 v131, v50, v54
	v_cvt_pk_fp8_f32 v128, v10, v14 op_sel:[0,0,1]
	v_cvt_pk_fp8_f32 v129, v26, v30 op_sel:[0,0,1]
	v_cvt_pk_fp8_f32 v130, v42, v46 op_sel:[0,0,1]
	v_cvt_pk_fp8_f32 v131, v58, v62 op_sel:[0,0,1]
	s_nop 0
	global_store_dwordx4 v140, v[128:131], s[20:21] offset:2048
	v_mul_f32_e32 v3, 0x42000000, v3
	v_mul_f32_e32 v7, 0x42000000, v7
	v_mul_f32_e32 v11, 0x42000000, v11
	v_mul_f32_e32 v15, 0x42000000, v15
	v_mul_f32_e32 v19, 0x42000000, v19
	v_mul_f32_e32 v23, 0x42000000, v23
	v_mul_f32_e32 v27, 0x42000000, v27
	v_mul_f32_e32 v31, 0x42000000, v31
	v_mul_f32_e32 v35, 0x42000000, v35
	v_mul_f32_e32 v39, 0x42000000, v39
	v_mul_f32_e32 v43, 0x42000000, v43
	v_mul_f32_e32 v47, 0x42000000, v47
	v_mul_f32_e32 v51, 0x42000000, v51
	v_mul_f32_e32 v55, 0x42000000, v55
	v_mul_f32_e32 v59, 0x42000000, v59
	v_mul_f32_e32 v63, 0x42000000, v63
	v_med3_f32 v3, v3, s28, v141
	v_med3_f32 v7, v7, s28, v141
	v_med3_f32 v11, v11, s28, v141
	v_med3_f32 v15, v15, s28, v141
	v_med3_f32 v19, v19, s28, v141
	v_med3_f32 v23, v23, s28, v141
	v_med3_f32 v27, v27, s28, v141
	v_med3_f32 v31, v31, s28, v141
	v_med3_f32 v35, v35, s28, v141
	v_med3_f32 v39, v39, s28, v141
	v_med3_f32 v43, v43, s28, v141
	v_med3_f32 v47, v47, s28, v141
	v_med3_f32 v51, v51, s28, v141
	v_med3_f32 v55, v55, s28, v141
	v_med3_f32 v59, v59, s28, v141
	v_med3_f32 v63, v63, s28, v141
	v_cvt_pk_fp8_f32 v132, v3, v7
	v_cvt_pk_fp8_f32 v133, v19, v23
	v_cvt_pk_fp8_f32 v134, v35, v39
	v_cvt_pk_fp8_f32 v135, v51, v55
	v_cvt_pk_fp8_f32 v132, v11, v15 op_sel:[0,0,1]
	v_cvt_pk_fp8_f32 v133, v27, v31 op_sel:[0,0,1]
	v_cvt_pk_fp8_f32 v134, v43, v47 op_sel:[0,0,1]
	v_cvt_pk_fp8_f32 v135, v59, v63 op_sel:[0,0,1]
	s_nop 0
	global_store_dwordx4 v140, v[132:135], s[20:21] offset:3072
	s_cmp_ge_u32 s7, s6
	s_cbranch_scc1 .Lp2c1_done
	s_mov_b32 s4, s7
.Lp2c1_loop:
	s_add_i32 s7, s4, s5
	s_cmp_lt_u32 s7, s6
	s_cbranch_scc0 .Lp2c1_B_last
	s_lshr_b32 s22, s7, 8
	s_and_b32 s23, s7, 0xff
	s_mov_b64 s[16:17], s[12:13]
	s_add_i32 s22, s22, 48
	s_lshl_b32 s24, s22, 22
	s_lshr_b32 s25, s23, 5
	s_lshl_b32 s25, s25, 19
	s_and_b32 s26, s23, 31
	s_lshl_b32 s26, s26, 7
	s_add_i32 s24, s24, s25
	s_add_i32 s24, s24, s26
	s_add_u32 s16, s16, s24
	s_addc_u32 s17, s17, 0
	s_nop 0
	global_load_dwordx4 v[0:3], v136, s[16:17] nt
	global_load_dwordx4 v[4:7], v137, s[16:17] nt
	global_load_dwordx4 v[8:11], v138, s[16:17] nt
	global_load_dwordx4 v[12:15], v139, s[16:17] nt
	s_add_u32 s16, s16, 0x4000
	s_addc_u32 s17, s17, 0
	s_nop 0
	global_load_dwordx4 v[16:19], v136, s[16:17] nt
	global_load_dwordx4 v[20:23], v137, s[16:17] nt
	global_load_dwordx4 v[24:27], v138, s[16:17] nt
	global_load_dwordx4 v[28:31], v139, s[16:17] nt
	s_add_u32 s16, s16, 0x4000
	s_addc_u32 s17, s17, 0
	s_nop 0
	global_load_dwordx4 v[32:35], v136, s[16:17] nt
	global_load_dwordx4 v[36:39], v137, s[16:17] nt
	global_load_dwordx4 v[40:43], v138, s[16:17] nt
	global_load_dwordx4 v[44:47], v139, s[16:17] nt
	s_add_u32 s16, s16, 0x4000
	s_addc_u32 s17, s17, 0
	s_nop 0
	global_load_dwordx4 v[48:51], v136, s[16:17] nt
	global_load_dwordx4 v[52:55], v137, s[16:17] nt
	global_load_dwordx4 v[56:59], v138, s[16:17] nt
	global_load_dwordx4 v[60:63], v139, s[16:17] nt
	s_waitcnt vmcnt(20)
	s_branch .Lp2c1_B_st

.Lp2c1_B_st:
	s_lshr_b32 s22, s4, 8
	s_and_b32 s23, s4, 0xff
	s_add_i32 s22, s22, 48
	s_mul_i32 s24, s22, 0x300000
	s_lshr_b32 s25, s23, 5
	s_lshl_b32 s25, s25, 7
	s_add_i32 s24, s24, s25
	s_and_b32 s26, s23, 31
	s_lshr_b32 s25, s26, 3
	s_lshl_b32 s25, s25, 18
	s_add_i32 s24, s24, s25
	s_bfe_u32 s25, s26, 0x20001
	s_lshl_b32 s25, s25, 15
	s_add_i32 s24, s24, s25
	s_and_b32 s25, s26, 1
	s_lshl_b32 s25, s25, 14
	s_add_i32 s24, s24, s25
	s_add_u32 s20, s10, s24
	s_addc_u32 s21, s11, 0
	v_mul_f32_e32 v64, 0x42000000, v64
	v_mul_f32_e32 v68, 0x42000000, v68
	v_mul_f32_e32 v72, 0x42000000, v72
	v_mul_f32_e32 v76, 0x42000000, v76
	v_mul_f32_e32 v80, 0x42000000, v80
	v_mul_f32_e32 v84, 0x42000000, v84
	v_mul_f32_e32 v88, 0x42000000, v88
	v_mul_f32_e32 v92, 0x42000000, v92
	v_mul_f32_e32 v96, 0x42000000, v96
	v_mul_f32_e32 v100, 0x42000000, v100
	v_mul_f32_e32 v104, 0x42000000, v104
	v_mul_f32_e32 v108, 0x42000000, v108
	v_mul_f32_e32 v112, 0x42000000, v112
	v_mul_f32_e32 v116, 0x42000000, v116
	v_mul_f32_e32 v120, 0x42000000, v120
	v_mul_f32_e32 v124, 0x42000000, v124
	v_med3_f32 v64, v64, s28, v141
	v_med3_f32 v68, v68, s28, v141
	v_med3_f32 v72, v72, s28, v141
	v_med3_f32 v76, v76, s28, v141
	v_med3_f32 v80, v80, s28, v141
	v_med3_f32 v84, v84, s28, v141
	v_med3_f32 v88, v88, s28, v141
	v_med3_f32 v92, v92, s28, v141
	v_med3_f32 v96, v96, s28, v141
	v_med3_f32 v100, v100, s28, v141
	v_med3_f32 v104, v104, s28, v141
	v_med3_f32 v108, v108, s28, v141
	v_med3_f32 v112, v112, s28, v141
	v_med3_f32 v116, v116, s28, v141
	v_med3_f32 v120, v120, s28, v141
	v_med3_f32 v124, v124, s28, v141
	v_cvt_pk_fp8_f32 v128, v64, v68
	v_cvt_pk_fp8_f32 v129, v80, v84
	v_cvt_pk_fp8_f32 v130, v96, v100
	v_cvt_pk_fp8_f32 v131, v112, v116
	v_cvt_pk_fp8_f32 v128, v72, v76 op_sel:[0,0,1]
	v_cvt_pk_fp8_f32 v129, v88, v92 op_sel:[0,0,1]
	v_cvt_pk_fp8_f32 v130, v104, v108 op_sel:[0,0,1]
	v_cvt_pk_fp8_f32 v131, v120, v124 op_sel:[0,0,1]
	s_nop 0
	global_store_dwordx4 v140, v[128:131], s[20:21]
	v_mul_f32_e32 v65, 0x42000000, v65
	v_mul_f32_e32 v69, 0x42000000, v69
	v_mul_f32_e32 v73, 0x42000000, v73
	v_mul_f32_e32 v77, 0x42000000, v77
	v_mul_f32_e32 v81, 0x42000000, v81
	v_mul_f32_e32 v85, 0x42000000, v85
	v_mul_f32_e32 v89, 0x42000000, v89
	v_mul_f32_e32 v93, 0x42000000, v93
	v_mul_f32_e32 v97, 0x42000000, v97
	v_mul_f32_e32 v101, 0x42000000, v101
	v_mul_f32_e32 v105, 0x42000000, v105
	v_mul_f32_e32 v109, 0x42000000, v109
	v_mul_f32_e32 v113, 0x42000000, v113
	v_mul_f32_e32 v117, 0x42000000, v117
	v_mul_f32_e32 v121, 0x42000000, v121
	v_mul_f32_e32 v125, 0x42000000, v125
	v_med3_f32 v65, v65, s28, v141
	v_med3_f32 v69, v69, s28, v141
	v_med3_f32 v73, v73, s28, v141
	v_med3_f32 v77, v77, s28, v141
	v_med3_f32 v81, v81, s28, v141
	v_med3_f32 v85, v85, s28, v141
	v_med3_f32 v89, v89, s28, v141
	v_med3_f32 v93, v93, s28, v141
	v_med3_f32 v97, v97, s28, v141
	v_med3_f32 v101, v101, s28, v141
	v_med3_f32 v105, v105, s28, v141
	v_med3_f32 v109, v109, s28, v141
	v_med3_f32 v113, v113, s28, v141
	v_med3_f32 v117, v117, s28, v141
	v_med3_f32 v121, v121, s28, v141
	v_med3_f32 v125, v125, s28, v141
	v_cvt_pk_fp8_f32 v132, v65, v69
	v_cvt_pk_fp8_f32 v133, v81, v85
	v_cvt_pk_fp8_f32 v134, v97, v101
	v_cvt_pk_fp8_f32 v135, v113, v117
	v_cvt_pk_fp8_f32 v132, v73, v77 op_sel:[0,0,1]
	v_cvt_pk_fp8_f32 v133, v89, v93 op_sel:[0,0,1]
	v_cvt_pk_fp8_f32 v134, v105, v109 op_sel:[0,0,1]
	v_cvt_pk_fp8_f32 v135, v121, v125 op_sel:[0,0,1]
	s_nop 0
	global_store_dwordx4 v140, v[132:135], s[20:21] offset:1024
	v_mul_f32_e32 v66, 0x42000000, v66
	v_mul_f32_e32 v70, 0x42000000, v70
	v_mul_f32_e32 v74, 0x42000000, v74
	v_mul_f32_e32 v78, 0x42000000, v78
	v_mul_f32_e32 v82, 0x42000000, v82
	v_mul_f32_e32 v86, 0x42000000, v86
	v_mul_f32_e32 v90, 0x42000000, v90
	v_mul_f32_e32 v94, 0x42000000, v94
	v_mul_f32_e32 v98, 0x42000000, v98
	v_mul_f32_e32 v102, 0x42000000, v102
	v_mul_f32_e32 v106, 0x42000000, v106
	v_mul_f32_e32 v110, 0x42000000, v110
	v_mul_f32_e32 v114, 0x42000000, v114
	v_mul_f32_e32 v118, 0x42000000, v118
	v_mul_f32_e32 v122, 0x42000000, v122
	v_mul_f32_e32 v126, 0x42000000, v126
	v_med3_f32 v66, v66, s28, v141
	v_med3_f32 v70, v70, s28, v141
	v_med3_f32 v74, v74, s28, v141
	v_med3_f32 v78, v78, s28, v141
	v_med3_f32 v82, v82, s28, v141
	v_med3_f32 v86, v86, s28, v141
	v_med3_f32 v90, v90, s28, v141
	v_med3_f32 v94, v94, s28, v141
	v_med3_f32 v98, v98, s28, v141
	v_med3_f32 v102, v102, s28, v141
	v_med3_f32 v106, v106, s28, v141
	v_med3_f32 v110, v110, s28, v141
	v_med3_f32 v114, v114, s28, v141
	v_med3_f32 v118, v118, s28, v141
	v_med3_f32 v122, v122, s28, v141
	v_med3_f32 v126, v126, s28, v141
	v_cvt_pk_fp8_f32 v128, v66, v70
	v_cvt_pk_fp8_f32 v129, v82, v86
	v_cvt_pk_fp8_f32 v130, v98, v102
	v_cvt_pk_fp8_f32 v131, v114, v118
	v_cvt_pk_fp8_f32 v128, v74, v78 op_sel:[0,0,1]
	v_cvt_pk_fp8_f32 v129, v90, v94 op_sel:[0,0,1]
	v_cvt_pk_fp8_f32 v130, v106, v110 op_sel:[0,0,1]
	v_cvt_pk_fp8_f32 v131, v122, v126 op_sel:[0,0,1]
	s_nop 0
	global_store_dwordx4 v140, v[128:131], s[20:21] offset:2048
	v_mul_f32_e32 v67, 0x42000000, v67
	v_mul_f32_e32 v71, 0x42000000, v71
	v_mul_f32_e32 v75, 0x42000000, v75
	v_mul_f32_e32 v79, 0x42000000, v79
	v_mul_f32_e32 v83, 0x42000000, v83
	v_mul_f32_e32 v87, 0x42000000, v87
	v_mul_f32_e32 v91, 0x42000000, v91
	v_mul_f32_e32 v95, 0x42000000, v95
	v_mul_f32_e32 v99, 0x42000000, v99
	v_mul_f32_e32 v103, 0x42000000, v103
	v_mul_f32_e32 v107, 0x42000000, v107
	v_mul_f32_e32 v111, 0x42000000, v111
	v_mul_f32_e32 v115, 0x42000000, v115
	v_mul_f32_e32 v119, 0x42000000, v119
	v_mul_f32_e32 v123, 0x42000000, v123
	v_mul_f32_e32 v127, 0x42000000, v127
	v_med3_f32 v67, v67, s28, v141
	v_med3_f32 v71, v71, s28, v141
	v_med3_f32 v75, v75, s28, v141
	v_med3_f32 v79, v79, s28, v141
	v_med3_f32 v83, v83, s28, v141
	v_med3_f32 v87, v87, s28, v141
	v_med3_f32 v91, v91, s28, v141
	v_med3_f32 v95, v95, s28, v141
	v_med3_f32 v99, v99, s28, v141
	v_med3_f32 v103, v103, s28, v141
	v_med3_f32 v107, v107, s28, v141
	v_med3_f32 v111, v111, s28, v141
	v_med3_f32 v115, v115, s28, v141
	v_med3_f32 v119, v119, s28, v141
	v_med3_f32 v123, v123, s28, v141
	v_med3_f32 v127, v127, s28, v141
	v_cvt_pk_fp8_f32 v132, v67, v71
	v_cvt_pk_fp8_f32 v133, v83, v87
	v_cvt_pk_fp8_f32 v134, v99, v103
	v_cvt_pk_fp8_f32 v135, v115, v119
	v_cvt_pk_fp8_f32 v132, v75, v79 op_sel:[0,0,1]
	v_cvt_pk_fp8_f32 v133, v91, v95 op_sel:[0,0,1]
	v_cvt_pk_fp8_f32 v134, v107, v111 op_sel:[0,0,1]
	v_cvt_pk_fp8_f32 v135, v123, v127 op_sel:[0,0,1]
	s_nop 0
	global_store_dwordx4 v140, v[132:135], s[20:21] offset:3072
	s_cmp_ge_u32 s7, s6
	s_cbranch_scc1 .Lp2c1_done
	s_mov_b32 s4, s7
	s_add_i32 s7, s4, s5
	s_cmp_lt_u32 s7, s6
	s_cbranch_scc0 .Lp2c1_A_last
	s_lshr_b32 s22, s7, 8
	s_and_b32 s23, s7, 0xff
	s_mov_b64 s[16:17], s[12:13]
	s_add_i32 s22, s22, 48
	s_lshl_b32 s24, s22, 22
	s_lshr_b32 s25, s23, 5
	s_lshl_b32 s25, s25, 19
	s_and_b32 s26, s23, 31
	s_lshl_b32 s26, s26, 7
	s_add_i32 s24, s24, s25
	s_add_i32 s24, s24, s26
	s_add_u32 s16, s16, s24
	s_addc_u32 s17, s17, 0
	s_nop 0
	global_load_dwordx4 v[64:67], v136, s[16:17] nt
	global_load_dwordx4 v[68:71], v137, s[16:17] nt
	global_load_dwordx4 v[72:75], v138, s[16:17] nt
	global_load_dwordx4 v[76:79], v139, s[16:17] nt
	s_add_u32 s16, s16, 0x4000
	s_addc_u32 s17, s17, 0
	s_nop 0
	global_load_dwordx4 v[80:83], v136, s[16:17] nt
	global_load_dwordx4 v[84:87], v137, s[16:17] nt
	global_load_dwordx4 v[88:91], v138, s[16:17] nt
	global_load_dwordx4 v[92:95], v139, s[16:17] nt
	s_add_u32 s16, s16, 0x4000
	s_addc_u32 s17, s17, 0
	s_nop 0
	global_load_dwordx4 v[96:99], v136, s[16:17] nt
	global_load_dwordx4 v[100:103], v137, s[16:17] nt
	global_load_dwordx4 v[104:107], v138, s[16:17] nt
	global_load_dwordx4 v[108:111], v139, s[16:17] nt
	s_add_u32 s16, s16, 0x4000
	s_addc_u32 s17, s17, 0
	s_nop 0
	global_load_dwordx4 v[112:115], v136, s[16:17] nt
	global_load_dwordx4 v[116:119], v137, s[16:17] nt
	global_load_dwordx4 v[120:123], v138, s[16:17] nt
	global_load_dwordx4 v[124:127], v139, s[16:17] nt
	s_waitcnt vmcnt(20)
	s_branch .Lp2c1_A_st

.Lp2c1_A_st:
	s_lshr_b32 s22, s4, 8
	s_and_b32 s23, s4, 0xff
	s_add_i32 s22, s22, 48
	s_mul_i32 s24, s22, 0x300000
	s_lshr_b32 s25, s23, 5
	s_lshl_b32 s25, s25, 7
	s_add_i32 s24, s24, s25
	s_and_b32 s26, s23, 31
	s_lshr_b32 s25, s26, 3
	s_lshl_b32 s25, s25, 18
	s_add_i32 s24, s24, s25
	s_bfe_u32 s25, s26, 0x20001
	s_lshl_b32 s25, s25, 15
	s_add_i32 s24, s24, s25
	s_and_b32 s25, s26, 1
	s_lshl_b32 s25, s25, 14
	s_add_i32 s24, s24, s25
	s_add_u32 s20, s10, s24
	s_addc_u32 s21, s11, 0
	v_mul_f32_e32 v0, 0x42000000, v0
	v_mul_f32_e32 v4, 0x42000000, v4
	v_mul_f32_e32 v8, 0x42000000, v8
	v_mul_f32_e32 v12, 0x42000000, v12
	v_mul_f32_e32 v16, 0x42000000, v16
	v_mul_f32_e32 v20, 0x42000000, v20
	v_mul_f32_e32 v24, 0x42000000, v24
	v_mul_f32_e32 v28, 0x42000000, v28
	v_mul_f32_e32 v32, 0x42000000, v32
	v_mul_f32_e32 v36, 0x42000000, v36
	v_mul_f32_e32 v40, 0x42000000, v40
	v_mul_f32_e32 v44, 0x42000000, v44
	v_mul_f32_e32 v48, 0x42000000, v48
	v_mul_f32_e32 v52, 0x42000000, v52
	v_mul_f32_e32 v56, 0x42000000, v56
	v_mul_f32_e32 v60, 0x42000000, v60
	v_med3_f32 v0, v0, s28, v141
	v_med3_f32 v4, v4, s28, v141
	v_med3_f32 v8, v8, s28, v141
	v_med3_f32 v12, v12, s28, v141
	v_med3_f32 v16, v16, s28, v141
	v_med3_f32 v20, v20, s28, v141
	v_med3_f32 v24, v24, s28, v141
	v_med3_f32 v28, v28, s28, v141
	v_med3_f32 v32, v32, s28, v141
	v_med3_f32 v36, v36, s28, v141
	v_med3_f32 v40, v40, s28, v141
	v_med3_f32 v44, v44, s28, v141
	v_med3_f32 v48, v48, s28, v141
	v_med3_f32 v52, v52, s28, v141
	v_med3_f32 v56, v56, s28, v141
	v_med3_f32 v60, v60, s28, v141
	v_cvt_pk_fp8_f32 v128, v0, v4
	v_cvt_pk_fp8_f32 v129, v16, v20
	v_cvt_pk_fp8_f32 v130, v32, v36
	v_cvt_pk_fp8_f32 v131, v48, v52
	v_cvt_pk_fp8_f32 v128, v8, v12 op_sel:[0,0,1]
	v_cvt_pk_fp8_f32 v129, v24, v28 op_sel:[0,0,1]
	v_cvt_pk_fp8_f32 v130, v40, v44 op_sel:[0,0,1]
	v_cvt_pk_fp8_f32 v131, v56, v60 op_sel:[0,0,1]
	s_nop 0
	global_store_dwordx4 v140, v[128:131], s[20:21]
	v_mul_f32_e32 v1, 0x42000000, v1
	v_mul_f32_e32 v5, 0x42000000, v5
	v_mul_f32_e32 v9, 0x42000000, v9
	v_mul_f32_e32 v13, 0x42000000, v13
	v_mul_f32_e32 v17, 0x42000000, v17
	v_mul_f32_e32 v21, 0x42000000, v21
	v_mul_f32_e32 v25, 0x42000000, v25
	v_mul_f32_e32 v29, 0x42000000, v29
	v_mul_f32_e32 v33, 0x42000000, v33
	v_mul_f32_e32 v37, 0x42000000, v37
	v_mul_f32_e32 v41, 0x42000000, v41
	v_mul_f32_e32 v45, 0x42000000, v45
	v_mul_f32_e32 v49, 0x42000000, v49
	v_mul_f32_e32 v53, 0x42000000, v53
	v_mul_f32_e32 v57, 0x42000000, v57
	v_mul_f32_e32 v61, 0x42000000, v61
	v_med3_f32 v1, v1, s28, v141
	v_med3_f32 v5, v5, s28, v141
	v_med3_f32 v9, v9, s28, v141
	v_med3_f32 v13, v13, s28, v141
	v_med3_f32 v17, v17, s28, v141
	v_med3_f32 v21, v21, s28, v141
	v_med3_f32 v25, v25, s28, v141
	v_med3_f32 v29, v29, s28, v141
	v_med3_f32 v33, v33, s28, v141
	v_med3_f32 v37, v37, s28, v141
	v_med3_f32 v41, v41, s28, v141
	v_med3_f32 v45, v45, s28, v141
	v_med3_f32 v49, v49, s28, v141
	v_med3_f32 v53, v53, s28, v141
	v_med3_f32 v57, v57, s28, v141
	v_med3_f32 v61, v61, s28, v141
	v_cvt_pk_fp8_f32 v132, v1, v5
	v_cvt_pk_fp8_f32 v133, v17, v21
	v_cvt_pk_fp8_f32 v134, v33, v37
	v_cvt_pk_fp8_f32 v135, v49, v53
	v_cvt_pk_fp8_f32 v132, v9, v13 op_sel:[0,0,1]
	v_cvt_pk_fp8_f32 v133, v25, v29 op_sel:[0,0,1]
	v_cvt_pk_fp8_f32 v134, v41, v45 op_sel:[0,0,1]
	v_cvt_pk_fp8_f32 v135, v57, v61 op_sel:[0,0,1]
	s_nop 0
	global_store_dwordx4 v140, v[132:135], s[20:21] offset:1024
	v_mul_f32_e32 v2, 0x42000000, v2
	v_mul_f32_e32 v6, 0x42000000, v6
	v_mul_f32_e32 v10, 0x42000000, v10
	v_mul_f32_e32 v14, 0x42000000, v14
	v_mul_f32_e32 v18, 0x42000000, v18
	v_mul_f32_e32 v22, 0x42000000, v22
	v_mul_f32_e32 v26, 0x42000000, v26
	v_mul_f32_e32 v30, 0x42000000, v30
	v_mul_f32_e32 v34, 0x42000000, v34
	v_mul_f32_e32 v38, 0x42000000, v38
	v_mul_f32_e32 v42, 0x42000000, v42
	v_mul_f32_e32 v46, 0x42000000, v46
	v_mul_f32_e32 v50, 0x42000000, v50
	v_mul_f32_e32 v54, 0x42000000, v54
	v_mul_f32_e32 v58, 0x42000000, v58
	v_mul_f32_e32 v62, 0x42000000, v62
	v_med3_f32 v2, v2, s28, v141
	v_med3_f32 v6, v6, s28, v141
	v_med3_f32 v10, v10, s28, v141
	v_med3_f32 v14, v14, s28, v141
	v_med3_f32 v18, v18, s28, v141
	v_med3_f32 v22, v22, s28, v141
	v_med3_f32 v26, v26, s28, v141
	v_med3_f32 v30, v30, s28, v141
	v_med3_f32 v34, v34, s28, v141
	v_med3_f32 v38, v38, s28, v141
	v_med3_f32 v42, v42, s28, v141
	v_med3_f32 v46, v46, s28, v141
	v_med3_f32 v50, v50, s28, v141
	v_med3_f32 v54, v54, s28, v141
	v_med3_f32 v58, v58, s28, v141
	v_med3_f32 v62, v62, s28, v141
	v_cvt_pk_fp8_f32 v128, v2, v6
	v_cvt_pk_fp8_f32 v129, v18, v22
	v_cvt_pk_fp8_f32 v130, v34, v38
	v_cvt_pk_fp8_f32 v131, v50, v54
	v_cvt_pk_fp8_f32 v128, v10, v14 op_sel:[0,0,1]
	v_cvt_pk_fp8_f32 v129, v26, v30 op_sel:[0,0,1]
	v_cvt_pk_fp8_f32 v130, v42, v46 op_sel:[0,0,1]
	v_cvt_pk_fp8_f32 v131, v58, v62 op_sel:[0,0,1]
	s_nop 0
	global_store_dwordx4 v140, v[128:131], s[20:21] offset:2048
	v_mul_f32_e32 v3, 0x42000000, v3
	v_mul_f32_e32 v7, 0x42000000, v7
	v_mul_f32_e32 v11, 0x42000000, v11
	v_mul_f32_e32 v15, 0x42000000, v15
	v_mul_f32_e32 v19, 0x42000000, v19
	v_mul_f32_e32 v23, 0x42000000, v23
	v_mul_f32_e32 v27, 0x42000000, v27
	v_mul_f32_e32 v31, 0x42000000, v31
	v_mul_f32_e32 v35, 0x42000000, v35
	v_mul_f32_e32 v39, 0x42000000, v39
	v_mul_f32_e32 v43, 0x42000000, v43
	v_mul_f32_e32 v47, 0x42000000, v47
	v_mul_f32_e32 v51, 0x42000000, v51
	v_mul_f32_e32 v55, 0x42000000, v55
	v_mul_f32_e32 v59, 0x42000000, v59
	v_mul_f32_e32 v63, 0x42000000, v63
	v_med3_f32 v3, v3, s28, v141
	v_med3_f32 v7, v7, s28, v141
	v_med3_f32 v11, v11, s28, v141
	v_med3_f32 v15, v15, s28, v141
	v_med3_f32 v19, v19, s28, v141
	v_med3_f32 v23, v23, s28, v141
	v_med3_f32 v27, v27, s28, v141
	v_med3_f32 v31, v31, s28, v141
	v_med3_f32 v35, v35, s28, v141
	v_med3_f32 v39, v39, s28, v141
	v_med3_f32 v43, v43, s28, v141
	v_med3_f32 v47, v47, s28, v141
	v_med3_f32 v51, v51, s28, v141
	v_med3_f32 v55, v55, s28, v141
	v_med3_f32 v59, v59, s28, v141
	v_med3_f32 v63, v63, s28, v141
	v_cvt_pk_fp8_f32 v132, v3, v7
	v_cvt_pk_fp8_f32 v133, v19, v23
	v_cvt_pk_fp8_f32 v134, v35, v39
	v_cvt_pk_fp8_f32 v135, v51, v55
	v_cvt_pk_fp8_f32 v132, v11, v15 op_sel:[0,0,1]
	v_cvt_pk_fp8_f32 v133, v27, v31 op_sel:[0,0,1]
	v_cvt_pk_fp8_f32 v134, v43, v47 op_sel:[0,0,1]
	v_cvt_pk_fp8_f32 v135, v59, v63 op_sel:[0,0,1]
	s_nop 0
	global_store_dwordx4 v140, v[132:135], s[20:21] offset:3072
	s_cmp_ge_u32 s7, s6
	s_cbranch_scc1 .Lp2c1_done
	s_mov_b32 s4, s7
	s_branch .Lp2c1_loop
.Lp2c1_done:
.LBB0_275:
	s_mov_b64 s[4:5], 0

.LBB0_740:
	s_load_dwordx4 s[0:3], s[8:9], 0x138
	s_waitcnt lgkmcnt(0)
	s_mov_b64 s[4:5], s[0:1]
	s_cmp_lt_i32 s4, 7
	s_cselect_b64 s[0:1], -1, 0
	s_cmp_gt_i32 s5, 6
	s_cselect_b64 s[2:3], -1, 0
	s_and_b64 s[0:1], s[0:1], s[2:3]
	s_andn2_b64 vcc, exec, s[0:1]
	s_cbranch_vccnz .LBB0_960
	s_mov_b64 s[0:1], s[8:9]
	v_mbcnt_lo_u32_b32 v135, -1, 0
	v_mbcnt_hi_u32_b32 v135, -1, v135
	s_load_dword s74, s[8:9], 0x148
	s_add_u32 s2, s8, 0x148
	v_readlane_b32 s4, v243, 0
	s_addc_u32 s3, s9, 0
	v_readlane_b32 s5, v243, 1
	s_waitcnt lgkmcnt(0)
	s_sub_i32 s18, s74, 32
	s_cmp_lt_i32 s4, s18
	s_mov_b64 s[4:5], -1
	s_cbranch_scc1 .LBB0_777
	v_readlane_b32 s4, v243, 0
	s_sub_i32 s4, s4, s18
	s_lshl_b32 s4, s4, 3
	s_add_i32 s19, s4, s94
	s_cmpk_gt_u32 s19, 0x2fff
	v_lshlrev_b32_e32 v141, 1, v135
	v_lshlrev_b32_e32 v140, 2, v135
	v_readlane_b32 s5, v243, 1
	s_cbranch_scc1 .LBB0_753
	s_load_dwordx2 s[4:5], s[0:1], 0x118
	s_load_dwordx2 s[8:9], s[0:1], 0x130
	s_lshl_b32 s6, s19, 14
	s_and_b32 s6, s6, 0x7c00000
	v_and_b32_e32 v132, -16, v141
	s_waitcnt lgkmcnt(0)
	s_add_u32 s10, s4, s6
	s_addc_u32 s11, s5, 0
	s_lshl_b32 s20, s19, 2
	s_and_b32 s6, s20, 0x380
	s_waitcnt vmcnt(0)
	v_add_u32_e32 v0, s6, v132
	v_ashrrev_i32_e32 v1, 31, v0
	v_lshlrev_b64 v[0:1], 12, v[0:1]
	s_lshl_b32 s6, s19, 7
	s_mov_b32 s7, 0
	v_lshl_add_u64 v[0:1], s[10:11], 0, v[0:1]
	s_and_b32 s6, s6, 0xf80
	v_and_b32_e32 v134, 28, v140
	v_lshl_add_u64 v[0:1], v[0:1], 0, s[6:7]
	v_mov_b32_e32 v137, 0
	v_lshlrev_b32_e32 v136, 2, v134
	v_lshl_add_u64 v[64:65], v[0:1], 0, v[136:137]
	s_movk_i32 s21, 0x2000
	v_add_co_u32_e32 v8, vcc, s21, v64
	s_movk_i32 s22, 0x4000
	s_nop 0
	v_addc_co_u32_e32 v9, vcc, 0, v65, vcc
	v_add_co_u32_e32 v16, vcc, s22, v64
	s_movk_i32 s23, 0x6000
	s_nop 0
	v_addc_co_u32_e32 v17, vcc, 0, v65, vcc
	v_add_co_u32_e32 v24, vcc, s23, v64
	s_mov_b32 s24, 0x8000
	s_nop 0
	v_addc_co_u32_e32 v25, vcc, 0, v65, vcc
	v_add_co_u32_e32 v32, vcc, s24, v64
	s_mov_b32 s25, 0xa000
	s_nop 0
	v_addc_co_u32_e32 v33, vcc, 0, v65, vcc
	v_add_co_u32_e32 v40, vcc, s25, v64
	s_mov_b32 s26, 0xc000
	s_nop 0
	v_addc_co_u32_e32 v41, vcc, 0, v65, vcc
	v_add_co_u32_e32 v48, vcc, s26, v64
	s_mov_b32 s6, 0xe000
	s_nop 0
	v_addc_co_u32_e32 v49, vcc, 0, v65, vcc
	v_add_co_u32_e32 v52, vcc, s6, v64
	s_mov_b32 s6, 0xf000
	s_nop 0
	v_addc_co_u32_e32 v53, vcc, 0, v65, vcc
	v_add_co_u32_e32 v66, vcc, s6, v64
	global_load_dwordx4 v[0:3], v[8:9], off offset:-4096 nt
	global_load_dwordx4 v[4:7], v[8:9], off nt
	s_nop 0
	global_load_dwordx4 v[8:11], v[16:17], off offset:-4096 nt
	global_load_dwordx4 v[12:15], v[16:17], off nt
	s_nop 0
	global_load_dwordx4 v[16:19], v[24:25], off offset:-4096 nt
	global_load_dwordx4 v[20:23], v[24:25], off nt
	s_nop 0
	global_load_dwordx4 v[24:27], v[32:33], off offset:-4096 nt
	global_load_dwordx4 v[28:31], v[32:33], off nt
	s_nop 0
	global_load_dwordx4 v[32:35], v[40:41], off offset:-4096 nt
	global_load_dwordx4 v[36:39], v[40:41], off nt
	s_nop 0
	global_load_dwordx4 v[40:43], v[48:49], off offset:-4096 nt
	global_load_dwordx4 v[44:47], v[48:49], off nt
	s_nop 0
	global_load_dwordx4 v[48:51], v[52:53], off offset:-4096 nt
	global_load_dwordx4 v[56:59], v[52:53], off nt
	v_addc_co_u32_e32 v67, vcc, 0, v65, vcc
	global_load_dwordx4 v[52:55], v[64:65], off nt
	global_load_dwordx4 v[60:63], v[66:67], off nt
	s_lshl_b32 s27, s19, 5
	s_add_u32 s29, s8, 0x2900000
	v_readlane_b32 s10, v243, 0
	s_addc_u32 s30, s9, 0
	s_lshl_b32 s6, s10, 3
	s_add_i32 s6, s94, s6
	s_lshl_b32 s10, s74, 3
	s_sub_i32 s6, s6, s10
	s_add_i32 s31, s6, 0x300
	s_lshr_b32 s6, s19, 8
	s_mul_hi_u32 s10, s6, 0x300000
	s_mul_i32 s6, s6, 0x300000
	s_add_u32 s8, s8, s6
	v_ashrrev_i32_e32 v133, 31, v132
	v_lshlrev_b32_e32 v64, 6, v135
	s_addc_u32 s9, s9, s10
	v_and_b32_e32 v142, 0x80, v64
	v_readlane_b32 s11, v243, 1
	v_lshl_add_u64 v[64:65], s[8:9], 0, v[132:133]
	s_mov_b64 s[8:9], 0x2b00c00
	s_mov_b32 s28, 0xb000
	v_lshl_add_u64 v[138:139], v[64:65], 0, s[8:9]
	s_mov_b32 s34, 0xc3e00000
	s_mov_b64 s[8:9], 0x200000
	s_mov_b32 s35, 0x200000
	s_mov_b64 s[10:11], 0x600000
	v_mov_b32_e32 v143, 0x304
	v_mov_b32_e32 v144, 0x43e00000
	s_branch .LBB0_746
.LBB0_744:
	v_mul_f32_e32 v128, 0x42000000, v108
	v_mul_f32_e32 v129, 0x42000000, v68
	v_med3_f32 v131, v128, s34, v144
	v_med3_f32 v129, v129, s34, v144
	v_mov_b32_e32 v128, v137
	v_cvt_pk_fp8_f32 v128, v131, v129
	v_mul_f32_e32 v130, 0x42000000, v64
	v_mul_f32_e32 v129, 0x42000000, v76
	v_med3_f32 v130, v130, s34, v144
	v_med3_f32 v129, v129, s34, v144
	v_cvt_pk_fp8_f32 v128, v130, v129 op_sel:[0,0,1]
	v_mul_f32_e32 v129, 0x42000000, v72
	v_mul_f32_e32 v130, 0x42000000, v84
	v_med3_f32 v145, v129, s34, v144
	v_med3_f32 v130, v130, s34, v144
	v_mov_b32_e32 v129, v137
	v_cvt_pk_fp8_f32 v129, v145, v130
	v_mul_f32_e32 v131, 0x42000000, v80
	v_mul_f32_e32 v130, 0x42000000, v92
	v_med3_f32 v131, v131, s34, v144
	v_med3_f32 v130, v130, s34, v144
	v_cvt_pk_fp8_f32 v129, v131, v130 op_sel:[0,0,1]
	v_mul_f32_e32 v130, 0x42000000, v88
	v_mul_f32_e32 v131, 0x42000000, v100
	v_med3_f32 v148, v130, s34, v144
	v_med3_f32 v131, v131, s34, v144
	v_mov_b32_e32 v130, v137
	v_cvt_pk_fp8_f32 v130, v148, v131
	v_mul_f32_e32 v145, 0x42000000, v96
	v_mul_f32_e32 v131, 0x42000000, v104
	s_lshr_b32 s12, s16, 8
	v_med3_f32 v145, v145, s34, v144
	v_med3_f32 v131, v131, s34, v144
	s_mul_hi_u32 s13, s12, 0x300000
	s_mul_i32 s12, s12, 0x300000
	v_cvt_pk_fp8_f32 v130, v145, v131 op_sel:[0,0,1]
	v_mul_f32_e32 v131, 0x42000000, v112
	v_mul_f32_e32 v145, 0x42000000, v116
	s_add_u32 s12, s29, s12
	v_med3_f32 v149, v131, s34, v144
	v_med3_f32 v145, v145, s34, v144
	v_mov_b32_e32 v131, v137
	s_addc_u32 s13, s30, s13
	v_cvt_pk_fp8_f32 v131, v149, v145
	s_add_u32 s12, s12, s6
	s_addc_u32 s13, s13, 0
	v_mul_f32_e32 v148, 0x42000000, v120
	v_mul_f32_e32 v145, 0x42000000, v124
	v_lshl_add_u64 v[146:147], s[12:13], 0, v[132:133]
	v_med3_f32 v148, v148, s34, v144
	v_med3_f32 v145, v145, s34, v144
	v_cvt_pk_fp8_f32 v131, v148, v145 op_sel:[0,0,1]
	v_lshl_add_u64 v[146:147], v[146:147], 0, v[136:137]
	v_mul_f32_e32 v136, 0x42000000, v109
	v_mul_f32_e32 v145, 0x42000000, v69
	v_lshl_add_u64 v[158:159], v[146:147], 0, s[8:9]
	v_add_co_u32_e32 v160, vcc, s35, v146
	v_med3_f32 v136, v136, s34, v144
	v_med3_f32 v145, v145, s34, v144
	v_mov_b32_e32 v146, v137
	v_cvt_pk_fp8_f32 v146, v136, v145
	v_addc_co_u32_e32 v161, vcc, 0, v147, vcc
	v_mul_f32_e32 v147, 0x42000000, v65
	v_mul_f32_e32 v136, 0x42000000, v77
	v_med3_f32 v145, v147, s34, v144
	v_med3_f32 v136, v136, s34, v144
	v_cvt_pk_fp8_f32 v146, v145, v136 op_sel:[0,0,1]
	v_mul_f32_e32 v136, 0x42000000, v73
	v_mul_f32_e32 v145, 0x42000000, v85
	v_med3_f32 v136, v136, s34, v144
	v_med3_f32 v145, v145, s34, v144
	v_mov_b32_e32 v147, v137
	v_cvt_pk_fp8_f32 v147, v136, v145
	v_mul_f32_e32 v148, 0x42000000, v81
	v_mul_f32_e32 v136, 0x42000000, v93
	v_med3_f32 v145, v148, s34, v144
	v_med3_f32 v136, v136, s34, v144
	v_cvt_pk_fp8_f32 v147, v145, v136 op_sel:[0,0,1]
	v_mul_f32_e32 v136, 0x42000000, v89
	v_mul_f32_e32 v145, 0x42000000, v101
	v_med3_f32 v136, v136, s34, v144
	v_med3_f32 v145, v145, s34, v144
	v_mov_b32_e32 v148, v137
	v_cvt_pk_fp8_f32 v148, v136, v145
	v_mul_f32_e32 v149, 0x42000000, v97
	v_mul_f32_e32 v136, 0x42000000, v105
	v_med3_f32 v145, v149, s34, v144
	v_med3_f32 v136, v136, s34, v144
	v_cvt_pk_fp8_f32 v148, v145, v136 op_sel:[0,0,1]
	v_mul_f32_e32 v136, 0x42000000, v113
	v_mul_f32_e32 v145, 0x42000000, v117
	v_med3_f32 v136, v136, s34, v144
	v_med3_f32 v145, v145, s34, v144
	v_mov_b32_e32 v149, v137
	v_cvt_pk_fp8_f32 v149, v136, v145
	v_mul_f32_e32 v150, 0x42000000, v121
	v_mul_f32_e32 v136, 0x42000000, v125
	v_med3_f32 v145, v150, s34, v144
	v_med3_f32 v136, v136, s34, v144
	v_cvt_pk_fp8_f32 v149, v145, v136 op_sel:[0,0,1]
	v_mul_f32_e32 v136, 0x42000000, v110
	v_mul_f32_e32 v145, 0x42000000, v70
	v_med3_f32 v136, v136, s34, v144
	v_med3_f32 v145, v145, s34, v144
	v_mov_b32_e32 v150, v137
	v_cvt_pk_fp8_f32 v150, v136, v145
	v_mul_f32_e32 v151, 0x42000000, v66
	v_mul_f32_e32 v136, 0x42000000, v78
	v_med3_f32 v145, v151, s34, v144
	v_med3_f32 v136, v136, s34, v144
	v_cvt_pk_fp8_f32 v150, v145, v136 op_sel:[0,0,1]
	v_mul_f32_e32 v136, 0x42000000, v74
	v_mul_f32_e32 v145, 0x42000000, v86
	v_med3_f32 v136, v136, s34, v144
	v_med3_f32 v145, v145, s34, v144
	v_mov_b32_e32 v151, v137
	v_cvt_pk_fp8_f32 v151, v136, v145
	v_mul_f32_e32 v152, 0x42000000, v82
	v_mul_f32_e32 v136, 0x42000000, v94
	v_med3_f32 v145, v152, s34, v144
	v_med3_f32 v136, v136, s34, v144
	v_cvt_pk_fp8_f32 v151, v145, v136 op_sel:[0,0,1]
	v_mul_f32_e32 v136, 0x42000000, v90
	v_mul_f32_e32 v145, 0x42000000, v102
	v_med3_f32 v136, v136, s34, v144
	v_med3_f32 v145, v145, s34, v144
	v_mov_b32_e32 v152, v137
	v_cvt_pk_fp8_f32 v152, v136, v145
	v_mul_f32_e32 v153, 0x42000000, v98
	v_mul_f32_e32 v136, 0x42000000, v106
	v_med3_f32 v145, v153, s34, v144
	v_med3_f32 v136, v136, s34, v144
	v_cvt_pk_fp8_f32 v152, v145, v136 op_sel:[0,0,1]
	v_mul_f32_e32 v136, 0x42000000, v114
	v_mul_f32_e32 v145, 0x42000000, v118
	v_med3_f32 v136, v136, s34, v144
	v_med3_f32 v145, v145, s34, v144
	v_mov_b32_e32 v153, v137
	v_cvt_pk_fp8_f32 v153, v136, v145
	v_mul_f32_e32 v154, 0x42000000, v122
	v_mul_f32_e32 v136, 0x42000000, v126
	v_med3_f32 v145, v154, s34, v144
	v_med3_f32 v136, v136, s34, v144
	v_cvt_pk_fp8_f32 v153, v145, v136 op_sel:[0,0,1]
	v_mul_f32_e32 v136, 0x42000000, v111
	v_mul_f32_e32 v145, 0x42000000, v71
	v_med3_f32 v136, v136, s34, v144
	v_med3_f32 v145, v145, s34, v144
	v_mov_b32_e32 v154, v137
	v_cvt_pk_fp8_f32 v154, v136, v145
	v_mul_f32_e32 v155, 0x42000000, v67
	v_mul_f32_e32 v136, 0x42000000, v79
	v_med3_f32 v145, v155, s34, v144
	v_med3_f32 v136, v136, s34, v144
	v_cvt_pk_fp8_f32 v154, v145, v136 op_sel:[0,0,1]
	v_mul_f32_e32 v136, 0x42000000, v75
	v_mul_f32_e32 v145, 0x42000000, v87
	v_med3_f32 v136, v136, s34, v144
	v_med3_f32 v145, v145, s34, v144
	v_mov_b32_e32 v155, v137
	v_cvt_pk_fp8_f32 v155, v136, v145
	v_mul_f32_e32 v156, 0x42000000, v83
	v_mul_f32_e32 v136, 0x42000000, v95
	v_med3_f32 v145, v156, s34, v144
	v_med3_f32 v136, v136, s34, v144
	v_cvt_pk_fp8_f32 v155, v145, v136 op_sel:[0,0,1]
	v_mul_f32_e32 v136, 0x42000000, v91
	v_mul_f32_e32 v145, 0x42000000, v103
	v_med3_f32 v136, v136, s34, v144
	v_med3_f32 v145, v145, s34, v144
	v_mov_b32_e32 v156, v137
	v_cvt_pk_fp8_f32 v156, v136, v145
	v_mul_f32_e32 v157, 0x42000000, v99
	v_mul_f32_e32 v136, 0x42000000, v107
	v_med3_f32 v145, v157, s34, v144
	v_med3_f32 v136, v136, s34, v144
	v_cvt_pk_fp8_f32 v156, v145, v136 op_sel:[0,0,1]
	v_mul_f32_e32 v136, 0x42000000, v115
	v_mul_f32_e32 v145, 0x42000000, v119
	v_med3_f32 v136, v136, s34, v144
	v_med3_f32 v145, v145, s34, v144
	v_mov_b32_e32 v157, v137
	v_cvt_pk_fp8_f32 v157, v136, v145
	v_mul_f32_e32 v162, 0x42000000, v123
	v_mul_f32_e32 v136, 0x42000000, v127
	s_addk_i32 s31, 0x200
	s_addk_i32 s20, 0x800
	s_addk_i32 s27, 0x4000
	v_med3_f32 v145, v162, s34, v144
	v_med3_f32 v136, v136, s34, v144
	s_cmpk_gt_i32 s36, 0x2dff
	v_cvt_pk_fp8_f32 v157, v145, v136 op_sel:[0,0,1]
	v_lshl_add_u64 v[138:139], v[138:139], 0, s[10:11]
	s_cselect_b64 s[14:15], -1, 0
	global_store_dwordx4 v[160:161], v[128:131], off
	global_store_dwordx4 v[158:159], v[146:149], off offset:1024
	global_store_dwordx4 v[158:159], v[150:153], off offset:2048
	global_store_dwordx4 v[158:159], v[154:157], off offset:3072

.LBB0_746:
	s_add_i32 s36, s31, 0xfffffe00
	s_cmpk_lt_i32 s36, 0x2f00
	s_cselect_b64 s[14:15], -1, 0
	s_mov_b64 s[16:17], -1
	s_and_b64 vcc, exec, s[14:15]
	s_cbranch_vccnz .LBB0_748
	s_and_b32 s6, s20, 0x380
	s_and_b32 s12, s27, 0x3e0
	s_mov_b64 s[16:17], 0

.LBB0_750:
	v_or_b32_e32 v128, s12, v134
	v_lshrrev_b32_e32 v128, 1, v128
	v_and_b32_e32 v128, 0x78, v128
	v_bitop3_b32 v129, s12, v143, v134 bitop3:0xc8
	v_or3_b32 v136, v142, v129, v128
	s_waitcnt vmcnt(1)
	v_mul_f32_e32 v128, 0x42000000, v52
	v_mul_f32_e32 v129, 0x42000000, v0
	v_med3_f32 v131, v128, s34, v144
	v_med3_f32 v129, v129, s34, v144
	v_mov_b32_e32 v128, v137
	v_cvt_pk_fp8_f32 v128, v131, v129
	v_mul_f32_e32 v130, 0x42000000, v4
	v_mul_f32_e32 v129, 0x42000000, v8
	v_med3_f32 v130, v130, s34, v144
	v_med3_f32 v129, v129, s34, v144
	v_cvt_pk_fp8_f32 v128, v130, v129 op_sel:[0,0,1]
	v_mul_f32_e32 v129, 0x42000000, v12
	v_mul_f32_e32 v130, 0x42000000, v16
	v_med3_f32 v145, v129, s34, v144
	v_med3_f32 v130, v130, s34, v144
	v_mov_b32_e32 v129, v137
	v_cvt_pk_fp8_f32 v129, v145, v130
	v_mul_f32_e32 v131, 0x42000000, v20
	v_mul_f32_e32 v130, 0x42000000, v24
	v_med3_f32 v131, v131, s34, v144
	v_med3_f32 v130, v130, s34, v144
	v_cvt_pk_fp8_f32 v129, v131, v130 op_sel:[0,0,1]
	v_mul_f32_e32 v130, 0x42000000, v28
	v_mul_f32_e32 v131, 0x42000000, v32
	v_med3_f32 v146, v130, s34, v144
	v_med3_f32 v131, v131, s34, v144
	v_mov_b32_e32 v130, v137
	v_cvt_pk_fp8_f32 v130, v146, v131
	v_mul_f32_e32 v145, 0x42000000, v36
	v_mul_f32_e32 v131, 0x42000000, v40
	v_med3_f32 v145, v145, s34, v144
	v_med3_f32 v131, v131, s34, v144
	v_cvt_pk_fp8_f32 v130, v145, v131 op_sel:[0,0,1]
	v_mul_f32_e32 v131, 0x42000000, v44
	v_mul_f32_e32 v145, 0x42000000, v48
	v_med3_f32 v147, v131, s34, v144
	v_med3_f32 v145, v145, s34, v144
	v_mov_b32_e32 v131, v137
	v_cvt_pk_fp8_f32 v131, v147, v145
	v_mul_f32_e32 v146, 0x42000000, v56
	s_waitcnt vmcnt(0)
	v_mul_f32_e32 v145, 0x42000000, v60
	v_med3_f32 v146, v146, s34, v144
	v_med3_f32 v145, v145, s34, v144
	v_lshlrev_b32_e32 v136, 10, v136
	v_cvt_pk_fp8_f32 v131, v146, v145 op_sel:[0,0,1]
	v_lshl_add_u64 v[146:147], v[136:137], 0, s[6:7]
	v_lshl_add_u64 v[158:159], v[138:139], 0, v[146:147]
	v_mul_f32_e32 v145, 0x42000000, v53
	v_mul_f32_e32 v146, 0x42000000, v1
	v_med3_f32 v145, v145, s34, v144
	v_med3_f32 v148, v146, s34, v144
	v_mov_b32_e32 v146, v137
	v_cvt_pk_fp8_f32 v146, v145, v148
	v_mul_f32_e32 v147, 0x42000000, v5
	v_mul_f32_e32 v145, 0x42000000, v9
	v_med3_f32 v147, v147, s34, v144
	v_med3_f32 v145, v145, s34, v144
	v_cvt_pk_fp8_f32 v146, v147, v145 op_sel:[0,0,1]
	v_mul_f32_e32 v145, 0x42000000, v13
	v_mul_f32_e32 v147, 0x42000000, v17
	v_med3_f32 v145, v145, s34, v144
	v_med3_f32 v149, v147, s34, v144
	v_mov_b32_e32 v147, v137
	v_cvt_pk_fp8_f32 v147, v145, v149
	v_mul_f32_e32 v148, 0x42000000, v21
	v_mul_f32_e32 v145, 0x42000000, v25
	v_med3_f32 v148, v148, s34, v144
	v_med3_f32 v145, v145, s34, v144
	v_cvt_pk_fp8_f32 v147, v148, v145 op_sel:[0,0,1]
	v_mul_f32_e32 v145, 0x42000000, v29
	v_mul_f32_e32 v148, 0x42000000, v33
	v_med3_f32 v145, v145, s34, v144
	v_med3_f32 v150, v148, s34, v144
	v_mov_b32_e32 v148, v137
	v_cvt_pk_fp8_f32 v148, v145, v150
	v_mul_f32_e32 v149, 0x42000000, v37
	v_mul_f32_e32 v145, 0x42000000, v41
	v_med3_f32 v149, v149, s34, v144
	v_med3_f32 v145, v145, s34, v144
	v_cvt_pk_fp8_f32 v148, v149, v145 op_sel:[0,0,1]
	v_mul_f32_e32 v145, 0x42000000, v45
	v_mul_f32_e32 v149, 0x42000000, v49
	v_med3_f32 v145, v145, s34, v144
	v_med3_f32 v151, v149, s34, v144
	v_mov_b32_e32 v149, v137
	v_cvt_pk_fp8_f32 v149, v145, v151
	v_mul_f32_e32 v150, 0x42000000, v57
	v_mul_f32_e32 v145, 0x42000000, v61
	v_med3_f32 v150, v150, s34, v144
	v_med3_f32 v145, v145, s34, v144
	v_cvt_pk_fp8_f32 v149, v150, v145 op_sel:[0,0,1]
	v_mul_f32_e32 v145, 0x42000000, v54
	v_mul_f32_e32 v150, 0x42000000, v2
	v_med3_f32 v145, v145, s34, v144
	v_med3_f32 v152, v150, s34, v144
	v_mov_b32_e32 v150, v137
	v_cvt_pk_fp8_f32 v150, v145, v152
	v_mul_f32_e32 v151, 0x42000000, v6
	v_mul_f32_e32 v145, 0x42000000, v10
	v_med3_f32 v151, v151, s34, v144
	v_med3_f32 v145, v145, s34, v144
	v_cvt_pk_fp8_f32 v150, v151, v145 op_sel:[0,0,1]
	v_mul_f32_e32 v145, 0x42000000, v14
	v_mul_f32_e32 v151, 0x42000000, v18
	v_med3_f32 v145, v145, s34, v144
	v_med3_f32 v153, v151, s34, v144
	v_mov_b32_e32 v151, v137
	v_cvt_pk_fp8_f32 v151, v145, v153
	v_mul_f32_e32 v152, 0x42000000, v22
	v_mul_f32_e32 v145, 0x42000000, v26
	v_med3_f32 v152, v152, s34, v144
	v_med3_f32 v145, v145, s34, v144
	v_cvt_pk_fp8_f32 v151, v152, v145 op_sel:[0,0,1]
	v_mul_f32_e32 v145, 0x42000000, v30
	v_mul_f32_e32 v152, 0x42000000, v34
	v_med3_f32 v145, v145, s34, v144
	v_med3_f32 v154, v152, s34, v144
	v_mov_b32_e32 v152, v137
	v_cvt_pk_fp8_f32 v152, v145, v154
	v_mul_f32_e32 v153, 0x42000000, v38
	v_mul_f32_e32 v145, 0x42000000, v42
	v_med3_f32 v153, v153, s34, v144
	v_med3_f32 v145, v145, s34, v144
	v_cvt_pk_fp8_f32 v152, v153, v145 op_sel:[0,0,1]
	v_mul_f32_e32 v145, 0x42000000, v46
	v_mul_f32_e32 v153, 0x42000000, v50
	v_med3_f32 v145, v145, s34, v144
	v_med3_f32 v155, v153, s34, v144
	v_mov_b32_e32 v153, v137
	v_cvt_pk_fp8_f32 v153, v145, v155
	v_mul_f32_e32 v154, 0x42000000, v58
	v_mul_f32_e32 v145, 0x42000000, v62
	v_med3_f32 v154, v154, s34, v144
	v_med3_f32 v145, v145, s34, v144
	v_cvt_pk_fp8_f32 v153, v154, v145 op_sel:[0,0,1]
	v_mul_f32_e32 v145, 0x42000000, v55
	v_mul_f32_e32 v154, 0x42000000, v3
	v_med3_f32 v145, v145, s34, v144
	v_med3_f32 v156, v154, s34, v144
	v_mov_b32_e32 v154, v137
	v_cvt_pk_fp8_f32 v154, v145, v156
	v_mul_f32_e32 v155, 0x42000000, v7
	v_mul_f32_e32 v145, 0x42000000, v11
	v_med3_f32 v155, v155, s34, v144
	v_med3_f32 v145, v145, s34, v144
	v_cvt_pk_fp8_f32 v154, v155, v145 op_sel:[0,0,1]
	v_mul_f32_e32 v145, 0x42000000, v15
	v_mul_f32_e32 v155, 0x42000000, v19
	v_med3_f32 v145, v145, s34, v144
	v_med3_f32 v157, v155, s34, v144
	v_mov_b32_e32 v155, v137
	v_cvt_pk_fp8_f32 v155, v145, v157
	v_mul_f32_e32 v156, 0x42000000, v23
	v_mul_f32_e32 v145, 0x42000000, v27
	v_med3_f32 v156, v156, s34, v144
	v_med3_f32 v145, v145, s34, v144
	v_cvt_pk_fp8_f32 v155, v156, v145 op_sel:[0,0,1]
	v_mul_f32_e32 v145, 0x42000000, v31
	v_mul_f32_e32 v156, 0x42000000, v35
	v_med3_f32 v145, v145, s34, v144
	v_med3_f32 v160, v156, s34, v144
	v_mov_b32_e32 v156, v137
	v_cvt_pk_fp8_f32 v156, v145, v160
	v_mul_f32_e32 v157, 0x42000000, v39
	v_mul_f32_e32 v145, 0x42000000, v43
	v_med3_f32 v157, v157, s34, v144
	v_med3_f32 v145, v145, s34, v144
	v_cvt_pk_fp8_f32 v156, v157, v145 op_sel:[0,0,1]
	v_mul_f32_e32 v145, 0x42000000, v47
	v_mul_f32_e32 v157, 0x42000000, v51
	v_med3_f32 v145, v145, s34, v144
	v_med3_f32 v161, v157, s34, v144
	v_mov_b32_e32 v157, v137
	v_cvt_pk_fp8_f32 v157, v145, v161
	v_mul_f32_e32 v160, 0x42000000, v59
	v_mul_f32_e32 v145, 0x42000000, v63
	v_med3_f32 v160, v160, s34, v144
	v_med3_f32 v145, v145, s34, v144
	v_cvt_pk_fp8_f32 v157, v160, v145 op_sel:[0,0,1]
	s_andn2_b64 vcc, exec, s[14:15]
	s_mov_b64 s[14:15], -1
	global_store_dwordx4 v[158:159], v[128:131], off offset:-3072
	global_store_dwordx4 v[158:159], v[146:149], off offset:-2048
	global_store_dwordx4 v[158:159], v[150:153], off offset:-1024
	global_store_dwordx4 v[158:159], v[154:157], off
	s_cbranch_vccnz .LBB0_745
	s_cmpk_gt_i32 s36, 0x2dff
	s_cbranch_scc1 .LBB0_744
	s_lshr_b32 s14, s31, 8
	s_mov_b32 s15, s7
	s_lshl_b64 s[14:15], s[14:15], 22
	v_add_u32_e32 v0, s6, v132
	s_add_u32 s14, s4, s14
	v_ashrrev_i32_e32 v1, 31, v0
	s_addc_u32 s15, s5, s15
	v_lshlrev_b64 v[0:1], 12, v[0:1]
	v_lshl_add_u64 v[0:1], s[14:15], 0, v[0:1]
	s_mov_b32 s13, s7
	v_lshl_add_u64 v[0:1], s[12:13], 2, v[0:1]
	v_lshlrev_b32_e32 v2, 2, v134
	v_mov_b32_e32 v3, v137
	v_lshl_add_u64 v[56:57], v[0:1], 0, v[2:3]
	v_add_co_u32_e32 v8, vcc, s21, v56
	s_nop 1
	v_addc_co_u32_e32 v9, vcc, 0, v57, vcc
	v_add_co_u32_e32 v16, vcc, s22, v56
	global_load_dwordx4 v[0:3], v[8:9], off offset:-4096 nt
	global_load_dwordx4 v[4:7], v[8:9], off nt
	v_addc_co_u32_e32 v17, vcc, 0, v57, vcc
	v_add_co_u32_e32 v24, vcc, s23, v56
	global_load_dwordx4 v[8:11], v[16:17], off offset:-4096 nt
	global_load_dwordx4 v[12:15], v[16:17], off nt
	v_addc_co_u32_e32 v25, vcc, 0, v57, vcc
	v_add_co_u32_e32 v32, vcc, s24, v56
	global_load_dwordx4 v[16:19], v[24:25], off offset:-4096 nt
	global_load_dwordx4 v[20:23], v[24:25], off nt
	v_addc_co_u32_e32 v33, vcc, 0, v57, vcc
	v_add_co_u32_e32 v40, vcc, s25, v56
	global_load_dwordx4 v[24:27], v[32:33], off offset:-4096 nt
	global_load_dwordx4 v[28:31], v[32:33], off nt
	v_addc_co_u32_e32 v41, vcc, 0, v57, vcc
	v_add_co_u32_e32 v44, vcc, s26, v56
	global_load_dwordx4 v[32:35], v[40:41], off offset:-4096 nt
	global_load_dwordx4 v[36:39], v[40:41], off nt
	v_addc_co_u32_e32 v45, vcc, 0, v57, vcc
	v_add_co_u32_e32 v48, vcc, 0xd000, v56
	global_load_dwordx4 v[40:43], v[44:45], off offset:-4096 nt
	s_nop 0
	global_load_dwordx4 v[44:47], v[44:45], off nt
	v_addc_co_u32_e32 v49, vcc, 0, v57, vcc
	v_add_co_u32_e32 v58, vcc, 0xe000, v56
	global_load_dwordx4 v[52:55], v[56:57], off nt
	s_nop 0
	global_load_dwordx4 v[48:51], v[48:49], off nt
	v_addc_co_u32_e32 v59, vcc, 0, v57, vcc
	v_add_co_u32_e32 v60, vcc, 0xf000, v56
	s_nop 1
	v_addc_co_u32_e32 v61, vcc, 0, v57, vcc
	global_load_dwordx4 v[56:59], v[58:59], off nt
	s_nop 0
	global_load_dwordx4 v[60:63], v[60:61], off nt
	s_branch .LBB0_744
